# MFMA block heads shortened: side-job fast/slow tests and half-tile skip branches taken before the barrier (own barrier copy per path), redundant lgkmcnt(0) after the barrier dropped
# speedup vs baseline: 1.0043x; 1.0043x over previous
.Lp1vg_wd_b2:
	s_waitcnt lgkmcnt(0)
	s_barrier
	s_setprio 1
	v_mfma_f32_16x16x32_bf16 v[74:77], v[158:161], v[174:177], v[74:77]
	v_mfma_f32_16x16x32_bf16 v[70:73], v[166:169], v[174:177], v[70:73]
	v_mfma_f32_16x16x32_bf16 v[58:61], v[158:161], v[182:185], v[58:61]
	v_mfma_f32_16x16x32_bf16 v[54:57], v[166:169], v[182:185], v[54:57]
	v_mfma_f32_16x16x32_bf16 v[42:45], v[158:161], v[190:193], v[42:45]
	v_mfma_f32_16x16x32_bf16 v[38:41], v[166:169], v[190:193], v[38:41]
	v_mfma_f32_16x16x32_bf16 v[26:29], v[158:161], v[198:201], v[26:29]
	v_mfma_f32_16x16x32_bf16 v[22:25], v[166:169], v[198:201], v[22:25]
	v_mfma_f32_16x16x32_bf16 v[74:77], v[162:165], v[178:181], v[74:77]
	v_mfma_f32_16x16x32_bf16 v[70:73], v[170:173], v[178:181], v[70:73]
	v_mfma_f32_16x16x32_bf16 v[58:61], v[162:165], v[186:189], v[58:61]
	v_mfma_f32_16x16x32_bf16 v[54:57], v[170:173], v[186:189], v[54:57]
	v_mfma_f32_16x16x32_bf16 v[42:45], v[162:165], v[194:197], v[42:45]
	v_mfma_f32_16x16x32_bf16 v[38:41], v[170:173], v[194:197], v[38:41]
	v_mfma_f32_16x16x32_bf16 v[26:29], v[162:165], v[202:205], v[26:29]
	v_mfma_f32_16x16x32_bf16 v[22:25], v[170:173], v[202:205], v[22:25]
	s_setprio 0
	s_setprio 1
	v_mfma_f32_16x16x32_bf16 v[66:69], v[142:145], v[174:177], v[66:69]
	v_mfma_f32_16x16x32_bf16 v[62:65], v[150:153], v[174:177], v[62:65]
	v_mfma_f32_16x16x32_bf16 v[50:53], v[142:145], v[182:185], v[50:53]
	v_mfma_f32_16x16x32_bf16 v[46:49], v[150:153], v[182:185], v[46:49]
	v_mfma_f32_16x16x32_bf16 v[34:37], v[142:145], v[190:193], v[34:37]
	v_mfma_f32_16x16x32_bf16 v[30:33], v[150:153], v[190:193], v[30:33]
	v_mfma_f32_16x16x32_bf16 v[18:21], v[142:145], v[198:201], v[18:21]
	v_mfma_f32_16x16x32_bf16 v[14:17], v[150:153], v[198:201], v[14:17]
	v_mfma_f32_16x16x32_bf16 v[66:69], v[146:149], v[178:181], v[66:69]
	v_mfma_f32_16x16x32_bf16 v[62:65], v[154:157], v[178:181], v[62:65]
	v_mfma_f32_16x16x32_bf16 v[50:53], v[146:149], v[186:189], v[50:53]
	v_mfma_f32_16x16x32_bf16 v[46:49], v[154:157], v[186:189], v[46:49]
	v_mfma_f32_16x16x32_bf16 v[34:37], v[146:149], v[194:197], v[34:37]
	v_mfma_f32_16x16x32_bf16 v[30:33], v[154:157], v[194:197], v[30:33]
	v_mfma_f32_16x16x32_bf16 v[18:21], v[146:149], v[202:205], v[18:21]
	v_mfma_f32_16x16x32_bf16 v[14:17], v[154:157], v[202:205], v[14:17]
	s_setprio 0
	s_barrier
	s_add_i32 s81, s81, 2
	s_add_u32 s54, s54, 0x100
	s_addc_u32 s55, s55, 0
	s_add_u32 s79, s79, 0x100
	s_addc_u32 s80, s80, 0
	s_cmp_gt_u32 s81, 29
	s_cbranch_scc1 .LBB0_180

; #define PG8_LAS __attribute__((address_space(3)))
;     __device__ __forceinline__ void issue(PG8_LAS unsigned char* lds0, int j, int tid, int wid) const {
;         const float* s0; unsigned char* d; addr(j, tid, s0, d);
;         __builtin_amdgcn_global_load_lds((const unsigned*)s0, (PG8_LAS unsigned*)(lds0 + stage + wid * 1024), 16, 0, 2);
;         __builtin_amdgcn_global_load_lds((const unsigned*)(s0 + ntot), (PG8_LAS unsigned*)(lds0 + stage + 8192 + wid * 1024), 16, 0, 2);
;     }
;     __device__ __forceinline__ void read(v4i_t& t0, v4i_t& t1, int tid, unsigned ldsb) const {
;         asm volatile("ds_read_b128 %0, %1" : "=&v"(t0) : "v"(ldsb + stage + 16u * (unsigned)tid) : "memory");
;         asm volatile("ds_read_b128 %0, %1" : "=&v"(t1) : "v"(ldsb + stage + 8192u + 16u * (unsigned)tid) : "memory");
;     }
;     __device__ __forceinline__ void finish(v4i_t& t0, v4i_t& t1, int j, int tid) const {
;         asm volatile("" : "+v"(t0), "+v"(t1));
;         const float* s0; unsigned char* d; addr(j, tid, s0, d);
;         const f32x4 r0 = __builtin_bit_cast(f32x4, t0) * 64.f, r1 = __builtin_bit_cast(f32x4, t1) * 64.f;
;         int w0 = 0, w1 = 0; w0 = __builtin_amdgcn_cvt_pk_fp8_f32(r0[0], r1[0], w0, false); w0 = __builtin_amdgcn_cvt_pk_fp8_f32(r0[1], r1[1], w0, true);
;         w1 = __builtin_amdgcn_cvt_pk_fp8_f32(r0[2], r1[2], w1, false); w1 = __builtin_amdgcn_cvt_pk_fp8_f32(r0[3], r1[3], w1, true);
;         typedef int v2is __attribute__((ext_vector_type(2))); __builtin_nontemporal_store((v2is){w0, w1}, (v2is*)d);
.Lp1vg_wd_a1:
	s_waitcnt lgkmcnt(0)
	s_cmp_lt_i32 s98, 0
	s_cbranch_scc1 .Lp1vg_mmslow_aB
	s_cmpk_gt_i32 s77, 0x5f
	s_cbranch_scc1 .Lp1vg_mmslow_aB
	s_barrier
	s_setprio 1
	v_mfma_f32_16x16x32_bf16 v[138:141], v[158:161], v[198:201], v[138:141]
	s_add_i32 s4, s98, s68
	s_lshr_b32 s2, s4, 31
	s_add_i32 s2, s4, s2
	v_mfma_f32_16x16x32_bf16 v[134:137], v[166:169], v[198:201], v[134:137]
	s_ashr_i32 s5, s2, 1
	s_ashr_i32 s2, s2, 11
	s_and_b32 s3, s5, 0x3ff
	v_mfma_f32_16x16x32_bf16 v[122:125], v[158:161], v[190:193], v[122:125]
	s_ashr_i32 s56, s2, 31
	s_lshl_b32 s2, s2, 10
	v_pk_mul_f32 v[6:7], v[6:7], s[40:41] op_sel_hi:[1,0]
	v_mfma_f32_16x16x32_bf16 v[118:121], v[166:169], v[190:193], v[118:121]
	v_pk_mul_f32 v[8:9], v[8:9], s[40:41] op_sel_hi:[1,0]
	v_pk_mul_f32 v[10:11], v[10:11], s[40:41] op_sel_hi:[1,0]
	v_pk_mul_f32 v[12:13], v[12:13], s[40:41] op_sel_hi:[1,0]
	v_mfma_f32_16x16x32_bf16 v[106:109], v[158:161], v[182:185], v[106:109]
	s_or_b32 s2, s2, s3
	v_cvt_pk_fp8_f32 v6, v6, v10
	s_mul_hi_u32 s3, s2, 0x2100
	v_mfma_f32_16x16x32_bf16 v[102:105], v[166:169], v[182:185], v[102:105]
	s_mulk_i32 s56, 0x2100
	v_cvt_pk_fp8_f32 v6, v7, v11 op_sel:[0,0,1]
	s_add_i32 s3, s3, s56
	v_mfma_f32_16x16x32_bf16 v[90:93], v[158:161], v[174:177], v[90:93]
	s_mulk_i32 s2, 0x2100
	v_cvt_pk_fp8_f32 v7, v8, v12
	v_readlane_b32 s101, v251, 49
	v_mfma_f32_16x16x32_bf16 v[86:89], v[166:169], v[174:177], v[86:89]
	s_add_u32 s2, s101, s2
	v_readlane_b32 s101, v251, 31
	s_addc_u32 s3, s101, s3
	v_mfma_f32_16x16x32_bf16 v[138:141], v[162:165], v[202:205], v[138:141]
	v_cvt_pk_fp8_f32 v7, v9, v13 op_sel:[0,0,1]
	v_lshl_or_b32 v226, s4, 11, v208
	s_lshl_b32 s56, s5, 12
	v_mfma_f32_16x16x32_bf16 v[134:137], v[170:173], v[202:205], v[134:137]
	v_subrev_u32_e32 v4, s56, v226
	v_ashrrev_i32_e32 v5, 31, v4
	v_lshl_add_u64 v[4:5], v[4:5], 1, s[2:3]
	v_mfma_f32_16x16x32_bf16 v[122:125], v[162:165], v[194:197], v[122:125]
	global_store_dwordx2 v[4:5], v[6:7], off nt
	s_add_i32 s4, s77, s68
	s_lshr_b32 s2, s4, 31
	v_mfma_f32_16x16x32_bf16 v[118:121], v[170:173], v[194:197], v[118:121]
	s_add_i32 s2, s4, s2
	s_ashr_i32 s5, s2, 1
	s_ashr_i32 s2, s2, 11
	v_mfma_f32_16x16x32_bf16 v[106:109], v[162:165], v[186:189], v[106:109]
	s_ashr_i32 s3, s2, 31
	s_lshl_b64 s[2:3], s[2:3], 25
	v_readlane_b32 s82, v251, 36
	v_mfma_f32_16x16x32_bf16 v[102:105], v[170:173], v[186:189], v[102:105]
	v_readlane_b32 s83, v251, 37
	s_add_u32 s2, s82, s2
	s_addc_u32 s3, s83, s3
	v_mfma_f32_16x16x32_bf16 v[90:93], v[162:165], v[178:181], v[90:93]
	s_lshl_b32 s82, s5, 15
	s_and_b32 s82, s82, 0x1ff8000
	s_add_u32 s82, s2, s82
	s_addc_u32 s83, s3, 0
	v_mfma_f32_16x16x32_bf16 v[86:89], v[170:173], v[178:181], v[86:89]
	s_setprio 0
	s_setprio 1
	s_lshl_b32 s2, s5, 12
	s_lshl_b32 s3, s4, 11
	s_sub_i32 s2, s3, s2
	v_mfma_f32_16x16x32_bf16 v[130:133], v[142:145], v[198:201], v[130:133]
	s_ashr_i32 s3, s2, 31
	s_lshl_b64 s[2:3], s[2:3], 2
	s_add_u32 s2, s82, s2
	s_addc_u32 s3, s83, s3
	v_mfma_f32_16x16x32_bf16 v[126:129], v[150:153], v[198:201], v[126:129]
	v_lshlrev_b32_e32 v2, 2, v208
	v_lshl_add_u64 v[4:5], s[2:3], 0, v[2:3]
	v_lshl_add_u64 v[4:5], v[4:5], 0, s[42:43]
	v_mfma_f32_16x16x32_bf16 v[114:117], v[142:145], v[190:193], v[114:117]
	global_load_dwordx4 v[6:9], v2, s[2:3] nt
	global_load_dwordx4 v[10:13], v[4:5], off nt
	s_mov_b32 s100, 3
	v_mfma_f32_16x16x32_bf16 v[110:113], v[150:153], v[190:193], v[110:113]
	s_mov_b32 s98, s77
	s_add_i32 s77, s77, 1
	s_add_u32 s4, s54, 0xfff80080
	s_addc_u32 s5, s55, -1
	v_mfma_f32_16x16x32_bf16 v[98:101], v[142:145], v[182:185], v[98:101]
	s_cmp_eq_u32 s81, 28
	s_cselect_b32 s5, s7, s5
	s_cselect_b32 s4, s33, s4
	s_cselect_b32 s57, s45, s80
	s_cselect_b32 s56, s47, s79
	v_mfma_f32_16x16x32_bf16 v[94:97], v[150:153], v[182:185], v[94:97]
	v_mfma_f32_16x16x32_bf16 v[82:85], v[142:145], v[174:177], v[82:85]
	v_mfma_f32_16x16x32_bf16 v[78:81], v[150:153], v[174:177], v[78:81]
	v_mfma_f32_16x16x32_bf16 v[130:133], v[146:149], v[202:205], v[130:133]
	v_mfma_f32_16x16x32_bf16 v[126:129], v[154:157], v[202:205], v[126:129]
	v_mfma_f32_16x16x32_bf16 v[114:117], v[146:149], v[194:197], v[114:117]
	v_mfma_f32_16x16x32_bf16 v[110:113], v[154:157], v[194:197], v[110:113]
	v_mfma_f32_16x16x32_bf16 v[98:101], v[146:149], v[186:189], v[98:101]
	v_mfma_f32_16x16x32_bf16 v[94:97], v[154:157], v[186:189], v[94:97]
	v_mfma_f32_16x16x32_bf16 v[82:85], v[146:149], v[178:181], v[82:85]
	v_mfma_f32_16x16x32_bf16 v[78:81], v[154:157], v[178:181], v[78:81]
	s_setprio 0
	s_branch .Lp1vg_mmjoin_a
.Lp1vg_mmslow_aB:
	s_barrier
.Lp1vg_mmslow_a:
	s_mov_b32 s100, 0
	s_cmp_lt_i32 s98, 0
	s_cbranch_scc1 .Lp1vg_nf_a
	s_add_i32 s4, s98, s68
	s_lshr_b32 s2, s4, 31
	s_add_i32 s2, s4, s2
	s_ashr_i32 s5, s2, 1
	s_ashr_i32 s2, s2, 11
	s_and_b32 s3, s5, 0x3ff
	s_ashr_i32 s56, s2, 31
	s_lshl_b32 s2, s2, 10
	v_pk_mul_f32 v[6:7], v[6:7], s[40:41] op_sel_hi:[1,0]
	v_pk_mul_f32 v[8:9], v[8:9], s[40:41] op_sel_hi:[1,0]
	v_pk_mul_f32 v[10:11], v[10:11], s[40:41] op_sel_hi:[1,0]
	v_pk_mul_f32 v[12:13], v[12:13], s[40:41] op_sel_hi:[1,0]
	s_or_b32 s2, s2, s3
	v_cvt_pk_fp8_f32 v6, v6, v10
	s_mul_hi_u32 s3, s2, 0x2100
	s_mulk_i32 s56, 0x2100
	v_cvt_pk_fp8_f32 v6, v7, v11 op_sel:[0,0,1]
	s_add_i32 s3, s3, s56
	s_mulk_i32 s2, 0x2100
	v_cvt_pk_fp8_f32 v7, v8, v12
	v_readlane_b32 s101, v251, 49
	s_add_u32 s2, s101, s2
	v_readlane_b32 s101, v251, 31
	s_addc_u32 s3, s101, s3
	v_cvt_pk_fp8_f32 v7, v9, v13 op_sel:[0,0,1]
	v_lshl_or_b32 v226, s4, 11, v208
	s_lshl_b32 s56, s5, 12
	v_subrev_u32_e32 v4, s56, v226
	v_ashrrev_i32_e32 v5, 31, v4
	v_lshl_add_u64 v[4:5], v[4:5], 1, s[2:3]
	global_store_dwordx2 v[4:5], v[6:7], off nt
	s_mov_b32 s100, 1

.Lp1vg_wd_a2:
	s_waitcnt lgkmcnt(0)
	s_barrier
	s_setprio 1
	v_mfma_f32_16x16x32_bf16 v[74:77], v[158:161], v[174:177], v[74:77]
	v_mfma_f32_16x16x32_bf16 v[70:73], v[166:169], v[174:177], v[70:73]
	v_mfma_f32_16x16x32_bf16 v[58:61], v[158:161], v[182:185], v[58:61]
	v_mfma_f32_16x16x32_bf16 v[54:57], v[166:169], v[182:185], v[54:57]
	v_mfma_f32_16x16x32_bf16 v[42:45], v[158:161], v[190:193], v[42:45]
	v_mfma_f32_16x16x32_bf16 v[38:41], v[166:169], v[190:193], v[38:41]
	v_mfma_f32_16x16x32_bf16 v[26:29], v[158:161], v[198:201], v[26:29]
	v_mfma_f32_16x16x32_bf16 v[22:25], v[166:169], v[198:201], v[22:25]
	v_mfma_f32_16x16x32_bf16 v[74:77], v[162:165], v[178:181], v[74:77]
	v_mfma_f32_16x16x32_bf16 v[70:73], v[170:173], v[178:181], v[70:73]
	v_mfma_f32_16x16x32_bf16 v[58:61], v[162:165], v[186:189], v[58:61]
	v_mfma_f32_16x16x32_bf16 v[54:57], v[170:173], v[186:189], v[54:57]
	v_mfma_f32_16x16x32_bf16 v[42:45], v[162:165], v[194:197], v[42:45]
	v_mfma_f32_16x16x32_bf16 v[38:41], v[170:173], v[194:197], v[38:41]
	v_mfma_f32_16x16x32_bf16 v[26:29], v[162:165], v[202:205], v[26:29]
	v_mfma_f32_16x16x32_bf16 v[22:25], v[170:173], v[202:205], v[22:25]
	s_setprio 0
	s_setprio 1
	v_mfma_f32_16x16x32_bf16 v[66:69], v[142:145], v[174:177], v[66:69]
	v_mfma_f32_16x16x32_bf16 v[62:65], v[150:153], v[174:177], v[62:65]
	v_mfma_f32_16x16x32_bf16 v[50:53], v[142:145], v[182:185], v[50:53]
	v_mfma_f32_16x16x32_bf16 v[46:49], v[150:153], v[182:185], v[46:49]
	v_mfma_f32_16x16x32_bf16 v[34:37], v[142:145], v[190:193], v[34:37]
	v_mfma_f32_16x16x32_bf16 v[30:33], v[150:153], v[190:193], v[30:33]
	v_mfma_f32_16x16x32_bf16 v[18:21], v[142:145], v[198:201], v[18:21]
	v_mfma_f32_16x16x32_bf16 v[14:17], v[150:153], v[198:201], v[14:17]
	v_mfma_f32_16x16x32_bf16 v[66:69], v[146:149], v[178:181], v[66:69]
	v_mfma_f32_16x16x32_bf16 v[62:65], v[154:157], v[178:181], v[62:65]
	v_mfma_f32_16x16x32_bf16 v[50:53], v[146:149], v[186:189], v[50:53]
	v_mfma_f32_16x16x32_bf16 v[46:49], v[154:157], v[186:189], v[46:49]
	v_mfma_f32_16x16x32_bf16 v[34:37], v[146:149], v[194:197], v[34:37]
	v_mfma_f32_16x16x32_bf16 v[30:33], v[154:157], v[194:197], v[30:33]
	v_mfma_f32_16x16x32_bf16 v[18:21], v[146:149], v[202:205], v[18:21]
	v_mfma_f32_16x16x32_bf16 v[14:17], v[154:157], v[202:205], v[14:17]
	s_setprio 0
	s_barrier
	v_add_u32_e32 v2, 0x18000, v209
	ds_read_b128 v[158:161], v2
	ds_read_b128 v[162:165], v2 offset:1024
	ds_read_b128 v[166:169], v2 offset:2048
	ds_read_b128 v[170:173], v2 offset:3072
	v_add_u32_e32 v2, 0x1c000, v209
	ds_read_b128 v[142:145], v2
	ds_read_b128 v[146:149], v2 offset:1024
	ds_read_b128 v[150:153], v2 offset:2048
	ds_read_b128 v[154:157], v2 offset:3072
	s_add_u32 s4, s4, 0x80000
	s_addc_u32 s5, s5, 0
	s_mov_b32 m0, s66
	v_lshl_add_u64 v[238:239], s[4:5], 0, v[210:211]
	ds_read_b128 v[198:201], v234 offset:32768
	ds_read_b128 v[202:205], v234 offset:33792
	ds_read_b128 v[190:193], v234 offset:34816
	ds_read_b128 v[194:197], v234 offset:35840
	ds_read_b128 v[182:185], v234 offset:36864
	ds_read_b128 v[186:189], v234 offset:37888
	ds_read_b128 v[174:177], v234 offset:38912
	ds_read_b128 v[178:181], v234 offset:39936
	global_load_lds_dwordx4 v[238:239], off
	v_lshl_add_u64 v[238:239], s[4:5], 0, v[214:215]
	s_mov_b32 m0, s67
	s_nop 0
	global_load_lds_dwordx4 v[238:239], off
	s_cmp_eq_u32 s100, 3
	s_cbranch_scc1 .Lp1vg_w11_b1
	s_cmp_eq_u32 s100, 2
	s_cbranch_scc1 .Lp1vg_wk2_b1
	s_waitcnt vmcnt(8)
	s_branch .Lp1vg_wd_b1

; #define PG8_LAS __attribute__((address_space(3)))
;     __device__ __forceinline__ void issue(PG8_LAS unsigned char* lds0, int j, int tid, int wid) const {
;         const float* s0; unsigned char* d; addr(j, tid, s0, d);
;         __builtin_amdgcn_global_load_lds((const unsigned*)s0, (PG8_LAS unsigned*)(lds0 + stage + wid * 1024), 16, 0, 2);
;         __builtin_amdgcn_global_load_lds((const unsigned*)(s0 + ntot), (PG8_LAS unsigned*)(lds0 + stage + 8192 + wid * 1024), 16, 0, 2);
;     }
;     __device__ __forceinline__ void read(v4i_t& t0, v4i_t& t1, int tid, unsigned ldsb) const {
;         asm volatile("ds_read_b128 %0, %1" : "=&v"(t0) : "v"(ldsb + stage + 16u * (unsigned)tid) : "memory");
;         asm volatile("ds_read_b128 %0, %1" : "=&v"(t1) : "v"(ldsb + stage + 8192u + 16u * (unsigned)tid) : "memory");
;     }
;     __device__ __forceinline__ void finish(v4i_t& t0, v4i_t& t1, int j, int tid) const {
;         asm volatile("" : "+v"(t0), "+v"(t1));
;         const float* s0; unsigned char* d; addr(j, tid, s0, d);
;         const f32x4 r0 = __builtin_bit_cast(f32x4, t0) * 64.f, r1 = __builtin_bit_cast(f32x4, t1) * 64.f;
;         int w0 = 0, w1 = 0; w0 = __builtin_amdgcn_cvt_pk_fp8_f32(r0[0], r1[0], w0, false); w0 = __builtin_amdgcn_cvt_pk_fp8_f32(r0[1], r1[1], w0, true);
;         w1 = __builtin_amdgcn_cvt_pk_fp8_f32(r0[2], r1[2], w1, false); w1 = __builtin_amdgcn_cvt_pk_fp8_f32(r0[3], r1[3], w1, true);
;         typedef int v2is __attribute__((ext_vector_type(2))); __builtin_nontemporal_store((v2is){w0, w1}, (v2is*)d);
.Lp1vg_wd_b1:
	s_waitcnt lgkmcnt(0)
	s_cmp_lt_i32 s99, 0
	s_cbranch_scc1 .Lp1vg_mmslow_b
	s_cmpk_gt_i32 s77, 0x5f
	s_cbranch_scc1 .Lp1vg_mmslow_b
	s_barrier
	s_setprio 1
	v_mfma_f32_16x16x32_bf16 v[138:141], v[158:161], v[198:201], v[138:141]
	s_add_i32 s4, s99, s68
	s_lshr_b32 s2, s4, 31
	s_add_i32 s2, s4, s2
	v_mfma_f32_16x16x32_bf16 v[134:137], v[166:169], v[198:201], v[134:137]
	s_ashr_i32 s5, s2, 1
	s_ashr_i32 s2, s2, 11
	s_and_b32 s3, s5, 0x3ff
	v_mfma_f32_16x16x32_bf16 v[122:125], v[158:161], v[190:193], v[122:125]
	s_ashr_i32 s82, s2, 31
	s_lshl_b32 s2, s2, 10
	v_pk_mul_f32 v[240:241], v[240:241], s[40:41] op_sel_hi:[1,0]
	v_mfma_f32_16x16x32_bf16 v[118:121], v[166:169], v[190:193], v[118:121]
	v_pk_mul_f32 v[242:243], v[242:243], s[40:41] op_sel_hi:[1,0]
	v_pk_mul_f32 v[244:245], v[244:245], s[40:41] op_sel_hi:[1,0]
	v_pk_mul_f32 v[246:247], v[246:247], s[40:41] op_sel_hi:[1,0]
	v_mfma_f32_16x16x32_bf16 v[106:109], v[158:161], v[182:185], v[106:109]
	s_or_b32 s2, s2, s3
	v_cvt_pk_fp8_f32 v240, v240, v244
	s_mul_hi_u32 s3, s2, 0x2100
	v_mfma_f32_16x16x32_bf16 v[102:105], v[166:169], v[182:185], v[102:105]
	s_mulk_i32 s82, 0x2100
	v_cvt_pk_fp8_f32 v240, v241, v245 op_sel:[0,0,1]
	s_add_i32 s3, s3, s82
	v_mfma_f32_16x16x32_bf16 v[90:93], v[158:161], v[174:177], v[90:93]
	s_mulk_i32 s2, 0x2100
	v_cvt_pk_fp8_f32 v241, v242, v246
	v_readlane_b32 s101, v251, 49
	v_mfma_f32_16x16x32_bf16 v[86:89], v[166:169], v[174:177], v[86:89]
	s_add_u32 s2, s101, s2
	v_readlane_b32 s101, v251, 31
	s_addc_u32 s3, s101, s3
	v_mfma_f32_16x16x32_bf16 v[138:141], v[162:165], v[202:205], v[138:141]
	v_cvt_pk_fp8_f32 v241, v243, v247 op_sel:[0,0,1]
	v_lshl_or_b32 v248, s4, 11, v208
	s_lshl_b32 s82, s5, 12
	v_mfma_f32_16x16x32_bf16 v[134:137], v[170:173], v[202:205], v[134:137]
	v_subrev_u32_e32 v238, s82, v248
	v_ashrrev_i32_e32 v239, 31, v238
	v_lshl_add_u64 v[238:239], v[238:239], 1, s[2:3]
	v_mfma_f32_16x16x32_bf16 v[122:125], v[162:165], v[194:197], v[122:125]
	global_store_dwordx2 v[238:239], v[240:241], off nt
	s_add_i32 s4, s77, s68
	s_lshr_b32 s2, s4, 31
	v_mfma_f32_16x16x32_bf16 v[118:121], v[170:173], v[194:197], v[118:121]
	s_add_i32 s2, s4, s2
	s_ashr_i32 s5, s2, 1
	s_ashr_i32 s2, s2, 11
	v_mfma_f32_16x16x32_bf16 v[106:109], v[162:165], v[186:189], v[106:109]
	s_ashr_i32 s3, s2, 31
	s_lshl_b64 s[2:3], s[2:3], 25
	v_readlane_b32 s84, v251, 36
	v_mfma_f32_16x16x32_bf16 v[102:105], v[170:173], v[186:189], v[102:105]
	v_readlane_b32 s85, v251, 37
	s_add_u32 s2, s84, s2
	s_addc_u32 s3, s85, s3
	v_mfma_f32_16x16x32_bf16 v[90:93], v[162:165], v[178:181], v[90:93]
	s_lshl_b32 s84, s5, 15
	s_and_b32 s84, s84, 0x1ff8000
	s_add_u32 s84, s2, s84
	s_addc_u32 s85, s3, 0
	v_mfma_f32_16x16x32_bf16 v[86:89], v[170:173], v[178:181], v[86:89]
	s_setprio 0
	s_setprio 1
	s_lshl_b32 s2, s5, 12
	s_lshl_b32 s3, s4, 11
	s_sub_i32 s2, s3, s2
	v_mfma_f32_16x16x32_bf16 v[130:133], v[142:145], v[198:201], v[130:133]
	s_ashr_i32 s3, s2, 31
	s_lshl_b64 s[2:3], s[2:3], 2
	s_add_u32 s2, s84, s2
	s_addc_u32 s3, s85, s3
	v_mfma_f32_16x16x32_bf16 v[126:129], v[150:153], v[198:201], v[126:129]
	v_lshlrev_b32_e32 v2, 2, v208
	v_lshl_add_u64 v[238:239], s[2:3], 0, v[2:3]
	v_lshl_add_u64 v[238:239], v[238:239], 0, s[42:43]
	v_mfma_f32_16x16x32_bf16 v[114:117], v[142:145], v[190:193], v[114:117]
	global_load_dwordx4 v[240:243], v2, s[2:3] nt
	global_load_dwordx4 v[244:247], v[238:239], off nt
	s_mov_b32 s100, 3
	v_mfma_f32_16x16x32_bf16 v[110:113], v[150:153], v[190:193], v[110:113]
	s_mov_b32 s99, s77
	s_add_i32 s77, s77, 1
	v_mfma_f32_16x16x32_bf16 v[98:101], v[142:145], v[182:185], v[98:101]
	v_mfma_f32_16x16x32_bf16 v[94:97], v[150:153], v[182:185], v[94:97]
	v_mfma_f32_16x16x32_bf16 v[82:85], v[142:145], v[174:177], v[82:85]
	v_mfma_f32_16x16x32_bf16 v[78:81], v[150:153], v[174:177], v[78:81]
	v_mfma_f32_16x16x32_bf16 v[130:133], v[146:149], v[202:205], v[130:133]
	v_mfma_f32_16x16x32_bf16 v[126:129], v[154:157], v[202:205], v[126:129]
	v_mfma_f32_16x16x32_bf16 v[114:117], v[146:149], v[194:197], v[114:117]
	v_mfma_f32_16x16x32_bf16 v[110:113], v[154:157], v[194:197], v[110:113]
	v_mfma_f32_16x16x32_bf16 v[98:101], v[146:149], v[186:189], v[98:101]
	v_mfma_f32_16x16x32_bf16 v[94:97], v[154:157], v[186:189], v[94:97]
	v_mfma_f32_16x16x32_bf16 v[82:85], v[146:149], v[178:181], v[82:85]
	v_mfma_f32_16x16x32_bf16 v[78:81], v[154:157], v[178:181], v[78:81]
	s_setprio 0
	s_branch .Lp1vg_mmafter_b

.Lp4vg_wd_b2:
	s_waitcnt lgkmcnt(0)
	s_barrier
	s_setprio 1
	v_mfma_f32_16x16x32_bf16 v[74:77], v[158:161], v[174:177], v[74:77]
	v_mfma_f32_16x16x32_bf16 v[70:73], v[166:169], v[174:177], v[70:73]
	v_mfma_f32_16x16x32_bf16 v[62:65], v[158:161], v[182:185], v[62:65]
	v_mfma_f32_16x16x32_bf16 v[58:61], v[166:169], v[182:185], v[58:61]
	v_mfma_f32_16x16x32_bf16 v[46:49], v[158:161], v[190:193], v[46:49]
	v_mfma_f32_16x16x32_bf16 v[42:45], v[166:169], v[190:193], v[42:45]
	v_mfma_f32_16x16x32_bf16 v[30:33], v[158:161], v[198:201], v[30:33]
	v_mfma_f32_16x16x32_bf16 v[26:29], v[166:169], v[198:201], v[26:29]
	v_mfma_f32_16x16x32_bf16 v[74:77], v[162:165], v[178:181], v[74:77]
	v_mfma_f32_16x16x32_bf16 v[70:73], v[170:173], v[178:181], v[70:73]
	v_mfma_f32_16x16x32_bf16 v[62:65], v[162:165], v[186:189], v[62:65]
	v_mfma_f32_16x16x32_bf16 v[58:61], v[170:173], v[186:189], v[58:61]
	v_mfma_f32_16x16x32_bf16 v[46:49], v[162:165], v[194:197], v[46:49]
	v_mfma_f32_16x16x32_bf16 v[42:45], v[170:173], v[194:197], v[42:45]
	v_mfma_f32_16x16x32_bf16 v[30:33], v[162:165], v[202:205], v[30:33]
	v_mfma_f32_16x16x32_bf16 v[26:29], v[170:173], v[202:205], v[26:29]
	s_setprio 0
	s_setprio 1
	v_mfma_f32_16x16x32_bf16 v[66:69], v[142:145], v[174:177], v[66:69]
	v_mfma_f32_16x16x32_bf16 v[54:57], v[150:153], v[174:177], v[54:57]
	v_mfma_f32_16x16x32_bf16 v[50:53], v[142:145], v[182:185], v[50:53]
	v_mfma_f32_16x16x32_bf16 v[38:41], v[150:153], v[182:185], v[38:41]
	v_mfma_f32_16x16x32_bf16 v[34:37], v[142:145], v[190:193], v[34:37]
	v_mfma_f32_16x16x32_bf16 v[22:25], v[150:153], v[190:193], v[22:25]
	v_mfma_f32_16x16x32_bf16 v[18:21], v[142:145], v[198:201], v[18:21]
	v_mfma_f32_16x16x32_bf16 v[14:17], v[150:153], v[198:201], v[14:17]
	v_mfma_f32_16x16x32_bf16 v[66:69], v[146:149], v[178:181], v[66:69]
	v_mfma_f32_16x16x32_bf16 v[54:57], v[154:157], v[178:181], v[54:57]
	v_mfma_f32_16x16x32_bf16 v[50:53], v[146:149], v[186:189], v[50:53]
	v_mfma_f32_16x16x32_bf16 v[38:41], v[154:157], v[186:189], v[38:41]
	v_mfma_f32_16x16x32_bf16 v[34:37], v[146:149], v[194:197], v[34:37]
	v_mfma_f32_16x16x32_bf16 v[22:25], v[154:157], v[194:197], v[22:25]
	v_mfma_f32_16x16x32_bf16 v[18:21], v[146:149], v[202:205], v[18:21]
	v_mfma_f32_16x16x32_bf16 v[14:17], v[154:157], v[202:205], v[14:17]
	s_setprio 0
	s_barrier
	s_add_i32 s60, s60, 2
	s_add_u32 s24, s24, 0x100
	s_addc_u32 s25, s25, 0
	s_add_u32 s58, s58, 0x100
	s_addc_u32 s59, s59, 0
	s_cmp_gt_u32 s60, 29
	s_cbranch_scc1 .LBB0_548

; #define PG8_LAS __attribute__((address_space(3)))
;     __device__ __forceinline__ void issue(PG8_LAS unsigned char* lds0, int j, int tid, int wid) const {
;         const float* s0; unsigned char* d; addr(j, tid, s0, d);
;         __builtin_amdgcn_global_load_lds((const unsigned*)s0, (PG8_LAS unsigned*)(lds0 + stage + wid * 1024), 16, 0, 2);
;         __builtin_amdgcn_global_load_lds((const unsigned*)(s0 + ntot), (PG8_LAS unsigned*)(lds0 + stage + 8192 + wid * 1024), 16, 0, 2);
;     }
;     __device__ __forceinline__ void read(v4i_t& t0, v4i_t& t1, int tid, unsigned ldsb) const {
;         asm volatile("ds_read_b128 %0, %1" : "=&v"(t0) : "v"(ldsb + stage + 16u * (unsigned)tid) : "memory");
;         asm volatile("ds_read_b128 %0, %1" : "=&v"(t1) : "v"(ldsb + stage + 8192u + 16u * (unsigned)tid) : "memory");
;     }
;     __device__ __forceinline__ void finish(v4i_t& t0, v4i_t& t1, int j, int tid) const {
;         asm volatile("" : "+v"(t0), "+v"(t1));
;         const float* s0; unsigned char* d; addr(j, tid, s0, d);
;         const f32x4 r0 = __builtin_bit_cast(f32x4, t0) * 64.f, r1 = __builtin_bit_cast(f32x4, t1) * 64.f;
;         int w0 = 0, w1 = 0; w0 = __builtin_amdgcn_cvt_pk_fp8_f32(r0[0], r1[0], w0, false); w0 = __builtin_amdgcn_cvt_pk_fp8_f32(r0[1], r1[1], w0, true);
;         w1 = __builtin_amdgcn_cvt_pk_fp8_f32(r0[2], r1[2], w1, false); w1 = __builtin_amdgcn_cvt_pk_fp8_f32(r0[3], r1[3], w1, true);
;         typedef int v2is __attribute__((ext_vector_type(2))); __builtin_nontemporal_store((v2is){w0, w1}, (v2is*)d);
.Lp4vg_wd_a1:
	s_waitcnt lgkmcnt(0)
	s_cmp_lt_i32 s98, 0
	s_cbranch_scc1 .Lp4vg_mmslow_aB
	s_cmp_gt_i32 s42, 31
	s_cbranch_scc1 .Lp4vg_mmslow_aB
	s_barrier
	s_setprio 1
	v_mfma_f32_16x16x32_bf16 v[138:141], v[158:161], v[198:201], v[138:141]
	s_add_i32 s22, s98, s47
	s_lshr_b32 s4, s22, 31
	s_add_i32 s4, s22, s4
	v_mfma_f32_16x16x32_bf16 v[134:137], v[166:169], v[198:201], v[134:137]
	s_ashr_i32 s23, s4, 1
	s_ashr_i32 s4, s4, 11
	s_and_b32 s5, s23, 0x3ff
	v_mfma_f32_16x16x32_bf16 v[126:129], v[158:161], v[190:193], v[126:129]
	s_ashr_i32 s34, s4, 31
	s_lshl_b32 s4, s4, 10
	v_pk_mul_f32 v[6:7], v[6:7], s[2:3] op_sel_hi:[1,0]
	v_mfma_f32_16x16x32_bf16 v[122:125], v[166:169], v[190:193], v[122:125]
	v_pk_mul_f32 v[8:9], v[8:9], s[2:3] op_sel_hi:[1,0]
	v_pk_mul_f32 v[10:11], v[10:11], s[2:3] op_sel_hi:[1,0]
	v_pk_mul_f32 v[12:13], v[12:13], s[2:3] op_sel_hi:[1,0]
	v_mfma_f32_16x16x32_bf16 v[110:113], v[158:161], v[182:185], v[110:113]
	s_or_b32 s4, s4, s5
	v_cvt_pk_fp8_f32 v6, v6, v10
	s_mul_hi_u32 s5, s4, 0x2100
	v_mfma_f32_16x16x32_bf16 v[106:109], v[166:169], v[182:185], v[106:109]
	s_mulk_i32 s34, 0x2100
	v_cvt_pk_fp8_f32 v6, v7, v11 op_sel:[0,0,1]
	s_add_i32 s5, s5, s34
	v_mfma_f32_16x16x32_bf16 v[94:97], v[158:161], v[174:177], v[94:97]
	s_mulk_i32 s4, 0x2100
	v_cvt_pk_fp8_f32 v7, v8, v12
	v_readlane_b32 s101, v251, 49
	v_mfma_f32_16x16x32_bf16 v[90:93], v[166:169], v[174:177], v[90:93]
	s_add_u32 s4, s101, s4
	v_readlane_b32 s101, v251, 31
	s_addc_u32 s5, s101, s5
	v_mfma_f32_16x16x32_bf16 v[138:141], v[162:165], v[202:205], v[138:141]
	v_cvt_pk_fp8_f32 v7, v9, v13 op_sel:[0,0,1]
	v_lshl_or_b32 v222, s22, 11, v208
	s_lshl_b32 s34, s23, 12
	v_mfma_f32_16x16x32_bf16 v[134:137], v[170:173], v[202:205], v[134:137]
	v_subrev_u32_e32 v4, s34, v222
	v_ashrrev_i32_e32 v5, 31, v4
	v_lshl_add_u64 v[4:5], v[4:5], 1, s[4:5]
	v_mfma_f32_16x16x32_bf16 v[126:129], v[162:165], v[194:197], v[126:129]
	global_store_dwordx2 v[4:5], v[6:7], off nt
	s_add_i32 s22, s42, s47
	s_lshr_b32 s4, s22, 31
	v_mfma_f32_16x16x32_bf16 v[122:125], v[170:173], v[194:197], v[122:125]
	s_add_i32 s4, s22, s4
	s_ashr_i32 s23, s4, 1
	s_ashr_i32 s4, s4, 11
	v_mfma_f32_16x16x32_bf16 v[110:113], v[162:165], v[186:189], v[110:113]
	s_ashr_i32 s5, s4, 31
	s_lshl_b64 s[4:5], s[4:5], 25
	v_readlane_b32 s34, v251, 36
	v_mfma_f32_16x16x32_bf16 v[106:109], v[170:173], v[186:189], v[106:109]
	v_readlane_b32 s35, v251, 37
	s_add_u32 s4, s34, s4
	s_addc_u32 s5, s35, s5
	v_mfma_f32_16x16x32_bf16 v[94:97], v[162:165], v[178:181], v[94:97]
	s_lshl_b32 s34, s23, 15
	s_and_b32 s34, s34, 0x1ff8000
	s_add_u32 s34, s4, s34
	s_addc_u32 s35, s5, 0
	v_mfma_f32_16x16x32_bf16 v[90:93], v[170:173], v[178:181], v[90:93]
	s_setprio 0
	s_setprio 1
	s_lshl_b32 s4, s23, 12
	s_lshl_b32 s5, s22, 11
	s_sub_i32 s4, s5, s4
	v_mfma_f32_16x16x32_bf16 v[130:133], v[142:145], v[198:201], v[130:133]
	s_ashr_i32 s5, s4, 31
	s_lshl_b64 s[4:5], s[4:5], 2
	s_add_u32 s4, s34, s4
	s_addc_u32 s5, s35, s5
	v_mfma_f32_16x16x32_bf16 v[118:121], v[150:153], v[198:201], v[118:121]
	v_lshlrev_b32_e32 v2, 2, v208
	v_lshl_add_u64 v[4:5], s[4:5], 0, v[2:3]
	v_lshl_add_u64 v[4:5], v[4:5], 0, s[8:9]
	v_mfma_f32_16x16x32_bf16 v[114:117], v[142:145], v[190:193], v[114:117]
	global_load_dwordx4 v[6:9], v2, s[4:5] nt
	global_load_dwordx4 v[10:13], v[4:5], off nt
	s_mov_b32 s100, 3
	v_mfma_f32_16x16x32_bf16 v[102:105], v[150:153], v[190:193], v[102:105]
	s_mov_b32 s98, s42
	s_add_i32 s42, s42, 1
	s_add_u32 s4, s24, 0xfff80080
	s_addc_u32 s5, s25, -1
	v_mfma_f32_16x16x32_bf16 v[98:101], v[142:145], v[182:185], v[98:101]
	s_cmp_eq_u32 s60, 28
	s_cselect_b32 s5, s11, s5
	s_cselect_b32 s4, s56, s4
	s_cselect_b32 s35, s15, s59
	s_cselect_b32 s34, s57, s58
	v_mfma_f32_16x16x32_bf16 v[86:89], v[150:153], v[182:185], v[86:89]
	v_mfma_f32_16x16x32_bf16 v[82:85], v[142:145], v[174:177], v[82:85]
	v_mfma_f32_16x16x32_bf16 v[78:81], v[150:153], v[174:177], v[78:81]
	v_mfma_f32_16x16x32_bf16 v[130:133], v[146:149], v[202:205], v[130:133]
	v_mfma_f32_16x16x32_bf16 v[118:121], v[154:157], v[202:205], v[118:121]
	v_mfma_f32_16x16x32_bf16 v[114:117], v[146:149], v[194:197], v[114:117]
	v_mfma_f32_16x16x32_bf16 v[102:105], v[154:157], v[194:197], v[102:105]
	v_mfma_f32_16x16x32_bf16 v[98:101], v[146:149], v[186:189], v[98:101]
	v_mfma_f32_16x16x32_bf16 v[86:89], v[154:157], v[186:189], v[86:89]
	v_mfma_f32_16x16x32_bf16 v[82:85], v[146:149], v[178:181], v[82:85]
	v_mfma_f32_16x16x32_bf16 v[78:81], v[154:157], v[178:181], v[78:81]
	s_setprio 0
	s_branch .Lp4vg_mmjoin_a
.Lp4vg_mmslow_aB:
	s_barrier
.Lp4vg_mmslow_a:
	s_mov_b32 s100, 0
	s_cmp_lt_i32 s98, 0
	s_cbranch_scc1 .Lp4vg_nf_a
	s_add_i32 s22, s98, s47
	s_lshr_b32 s4, s22, 31
	s_add_i32 s4, s22, s4
	s_ashr_i32 s23, s4, 1
	s_ashr_i32 s4, s4, 11
	s_and_b32 s5, s23, 0x3ff
	s_ashr_i32 s34, s4, 31
	s_lshl_b32 s4, s4, 10
	v_pk_mul_f32 v[6:7], v[6:7], s[2:3] op_sel_hi:[1,0]
	v_pk_mul_f32 v[8:9], v[8:9], s[2:3] op_sel_hi:[1,0]
	v_pk_mul_f32 v[10:11], v[10:11], s[2:3] op_sel_hi:[1,0]
	v_pk_mul_f32 v[12:13], v[12:13], s[2:3] op_sel_hi:[1,0]
	s_or_b32 s4, s4, s5
	v_cvt_pk_fp8_f32 v6, v6, v10
	s_mul_hi_u32 s5, s4, 0x2100
	s_mulk_i32 s34, 0x2100
	v_cvt_pk_fp8_f32 v6, v7, v11 op_sel:[0,0,1]
	s_add_i32 s5, s5, s34
	s_mulk_i32 s4, 0x2100
	v_cvt_pk_fp8_f32 v7, v8, v12
	v_readlane_b32 s101, v251, 49
	s_add_u32 s4, s101, s4
	v_readlane_b32 s101, v251, 31
	s_addc_u32 s5, s101, s5
	v_cvt_pk_fp8_f32 v7, v9, v13 op_sel:[0,0,1]
	v_lshl_or_b32 v222, s22, 11, v208
	s_lshl_b32 s34, s23, 12
	v_subrev_u32_e32 v4, s34, v222
	v_ashrrev_i32_e32 v5, 31, v4
	v_lshl_add_u64 v[4:5], v[4:5], 1, s[4:5]
	global_store_dwordx2 v[4:5], v[6:7], off nt
	s_mov_b32 s100, 1

.Lp4vg_wd_a2:
	s_waitcnt lgkmcnt(0)
	s_barrier
	s_setprio 1
	v_mfma_f32_16x16x32_bf16 v[74:77], v[158:161], v[174:177], v[74:77]
	v_mfma_f32_16x16x32_bf16 v[70:73], v[166:169], v[174:177], v[70:73]
	v_mfma_f32_16x16x32_bf16 v[62:65], v[158:161], v[182:185], v[62:65]
	v_mfma_f32_16x16x32_bf16 v[58:61], v[166:169], v[182:185], v[58:61]
	v_mfma_f32_16x16x32_bf16 v[46:49], v[158:161], v[190:193], v[46:49]
	v_mfma_f32_16x16x32_bf16 v[42:45], v[166:169], v[190:193], v[42:45]
	v_mfma_f32_16x16x32_bf16 v[30:33], v[158:161], v[198:201], v[30:33]
	v_mfma_f32_16x16x32_bf16 v[26:29], v[166:169], v[198:201], v[26:29]
	v_mfma_f32_16x16x32_bf16 v[74:77], v[162:165], v[178:181], v[74:77]
	v_mfma_f32_16x16x32_bf16 v[70:73], v[170:173], v[178:181], v[70:73]
	v_mfma_f32_16x16x32_bf16 v[62:65], v[162:165], v[186:189], v[62:65]
	v_mfma_f32_16x16x32_bf16 v[58:61], v[170:173], v[186:189], v[58:61]
	v_mfma_f32_16x16x32_bf16 v[46:49], v[162:165], v[194:197], v[46:49]
	v_mfma_f32_16x16x32_bf16 v[42:45], v[170:173], v[194:197], v[42:45]
	v_mfma_f32_16x16x32_bf16 v[30:33], v[162:165], v[202:205], v[30:33]
	v_mfma_f32_16x16x32_bf16 v[26:29], v[170:173], v[202:205], v[26:29]
	s_setprio 0
	s_setprio 1
	v_mfma_f32_16x16x32_bf16 v[66:69], v[142:145], v[174:177], v[66:69]
	v_mfma_f32_16x16x32_bf16 v[54:57], v[150:153], v[174:177], v[54:57]
	v_mfma_f32_16x16x32_bf16 v[50:53], v[142:145], v[182:185], v[50:53]
	v_mfma_f32_16x16x32_bf16 v[38:41], v[150:153], v[182:185], v[38:41]
	v_mfma_f32_16x16x32_bf16 v[34:37], v[142:145], v[190:193], v[34:37]
	v_mfma_f32_16x16x32_bf16 v[22:25], v[150:153], v[190:193], v[22:25]
	v_mfma_f32_16x16x32_bf16 v[18:21], v[142:145], v[198:201], v[18:21]
	v_mfma_f32_16x16x32_bf16 v[14:17], v[150:153], v[198:201], v[14:17]
	v_mfma_f32_16x16x32_bf16 v[66:69], v[146:149], v[178:181], v[66:69]
	v_mfma_f32_16x16x32_bf16 v[54:57], v[154:157], v[178:181], v[54:57]
	v_mfma_f32_16x16x32_bf16 v[50:53], v[146:149], v[186:189], v[50:53]
	v_mfma_f32_16x16x32_bf16 v[38:41], v[154:157], v[186:189], v[38:41]
	v_mfma_f32_16x16x32_bf16 v[34:37], v[146:149], v[194:197], v[34:37]
	v_mfma_f32_16x16x32_bf16 v[22:25], v[154:157], v[194:197], v[22:25]
	v_mfma_f32_16x16x32_bf16 v[18:21], v[146:149], v[202:205], v[18:21]
	v_mfma_f32_16x16x32_bf16 v[14:17], v[154:157], v[202:205], v[14:17]
	s_setprio 0
	s_barrier
	v_add_u32_e32 v2, 0x18000, v1
	ds_read_b128 v[158:161], v2
	ds_read_b128 v[162:165], v2 offset:1024
	ds_read_b128 v[166:169], v2 offset:2048
	ds_read_b128 v[170:173], v2 offset:3072
	v_add_u32_e32 v2, 0x1c000, v1
	ds_read_b128 v[142:145], v2
	ds_read_b128 v[146:149], v2 offset:1024
	ds_read_b128 v[150:153], v2 offset:2048
	ds_read_b128 v[154:157], v2 offset:3072
	s_add_u32 s4, s4, 0x80000
	s_addc_u32 s5, s5, 0
	s_mov_b32 m0, s44
	v_lshl_add_u64 v[232:233], s[4:5], 0, v[210:211]
	ds_read_b128 v[198:201], v230 offset:32768
	ds_read_b128 v[202:205], v230 offset:33792
	ds_read_b128 v[190:193], v230 offset:34816
	ds_read_b128 v[194:197], v230 offset:35840
	ds_read_b128 v[182:185], v230 offset:36864
	ds_read_b128 v[186:189], v230 offset:37888
	ds_read_b128 v[174:177], v230 offset:38912
	ds_read_b128 v[178:181], v230 offset:39936
	global_load_lds_dwordx4 v[232:233], off
	v_lshl_add_u64 v[232:233], s[4:5], 0, v[212:213]
	s_mov_b32 m0, s46
	s_nop 0
	global_load_lds_dwordx4 v[232:233], off
	s_cmp_eq_u32 s100, 3
	s_cbranch_scc1 .Lp4vg_w11_b1
	s_cmp_eq_u32 s100, 2
	s_cbranch_scc1 .Lp4vg_wk2_b1
	s_waitcnt vmcnt(8)
	s_branch .Lp4vg_wd_b1

; #define PG8_LAS __attribute__((address_space(3)))
;     __device__ __forceinline__ void issue(PG8_LAS unsigned char* lds0, int j, int tid, int wid) const {
;         const float* s0; unsigned char* d; addr(j, tid, s0, d);
;         __builtin_amdgcn_global_load_lds((const unsigned*)s0, (PG8_LAS unsigned*)(lds0 + stage + wid * 1024), 16, 0, 2);
;         __builtin_amdgcn_global_load_lds((const unsigned*)(s0 + ntot), (PG8_LAS unsigned*)(lds0 + stage + 8192 + wid * 1024), 16, 0, 2);
;     }
;     __device__ __forceinline__ void read(v4i_t& t0, v4i_t& t1, int tid, unsigned ldsb) const {
;         asm volatile("ds_read_b128 %0, %1" : "=&v"(t0) : "v"(ldsb + stage + 16u * (unsigned)tid) : "memory");
;         asm volatile("ds_read_b128 %0, %1" : "=&v"(t1) : "v"(ldsb + stage + 8192u + 16u * (unsigned)tid) : "memory");
;     }
;     __device__ __forceinline__ void finish(v4i_t& t0, v4i_t& t1, int j, int tid) const {
;         asm volatile("" : "+v"(t0), "+v"(t1));
;         const float* s0; unsigned char* d; addr(j, tid, s0, d);
;         const f32x4 r0 = __builtin_bit_cast(f32x4, t0) * 64.f, r1 = __builtin_bit_cast(f32x4, t1) * 64.f;
;         int w0 = 0, w1 = 0; w0 = __builtin_amdgcn_cvt_pk_fp8_f32(r0[0], r1[0], w0, false); w0 = __builtin_amdgcn_cvt_pk_fp8_f32(r0[1], r1[1], w0, true);
;         w1 = __builtin_amdgcn_cvt_pk_fp8_f32(r0[2], r1[2], w1, false); w1 = __builtin_amdgcn_cvt_pk_fp8_f32(r0[3], r1[3], w1, true);
;         typedef int v2is __attribute__((ext_vector_type(2))); __builtin_nontemporal_store((v2is){w0, w1}, (v2is*)d);
.Lp4vg_wd_b1:
	s_waitcnt lgkmcnt(0)
	s_cmp_lt_i32 s99, 0
	s_cbranch_scc1 .Lp4vg_mmslow_b
	s_cmp_gt_i32 s42, 31
	s_cbranch_scc1 .Lp4vg_mmslow_b
	s_barrier
	s_setprio 1
	v_mfma_f32_16x16x32_bf16 v[138:141], v[158:161], v[198:201], v[138:141]
	s_add_i32 s22, s99, s47
	s_lshr_b32 s4, s22, 31
	s_add_i32 s4, s22, s4
	v_mfma_f32_16x16x32_bf16 v[134:137], v[166:169], v[198:201], v[134:137]
	s_ashr_i32 s23, s4, 1
	s_ashr_i32 s4, s4, 11
	s_and_b32 s5, s23, 0x3ff
	v_mfma_f32_16x16x32_bf16 v[126:129], v[158:161], v[190:193], v[126:129]
	s_ashr_i32 s61, s4, 31
	s_lshl_b32 s4, s4, 10
	v_pk_mul_f32 v[242:243], v[242:243], s[2:3] op_sel_hi:[1,0]
	v_mfma_f32_16x16x32_bf16 v[122:125], v[166:169], v[190:193], v[122:125]
	v_pk_mul_f32 v[244:245], v[244:245], s[2:3] op_sel_hi:[1,0]
	v_pk_mul_f32 v[246:247], v[246:247], s[2:3] op_sel_hi:[1,0]
	v_pk_mul_f32 v[248:249], v[248:249], s[2:3] op_sel_hi:[1,0]
	v_mfma_f32_16x16x32_bf16 v[110:113], v[158:161], v[182:185], v[110:113]
	s_or_b32 s4, s4, s5
	v_cvt_pk_fp8_f32 v242, v242, v246
	s_mul_hi_u32 s5, s4, 0x2100
	v_mfma_f32_16x16x32_bf16 v[106:109], v[166:169], v[182:185], v[106:109]
	s_mulk_i32 s61, 0x2100
	v_cvt_pk_fp8_f32 v242, v243, v247 op_sel:[0,0,1]
	s_add_i32 s5, s5, s61
	v_mfma_f32_16x16x32_bf16 v[94:97], v[158:161], v[174:177], v[94:97]
	s_mulk_i32 s4, 0x2100
	v_cvt_pk_fp8_f32 v243, v244, v248
	v_readlane_b32 s101, v251, 49
	v_mfma_f32_16x16x32_bf16 v[90:93], v[166:169], v[174:177], v[90:93]
	s_add_u32 s4, s101, s4
	v_readlane_b32 s101, v251, 31
	s_addc_u32 s5, s101, s5
	v_mfma_f32_16x16x32_bf16 v[138:141], v[162:165], v[202:205], v[138:141]
	v_cvt_pk_fp8_f32 v243, v245, v249 op_sel:[0,0,1]
	v_lshl_or_b32 v234, s22, 11, v208
	s_lshl_b32 s61, s23, 12
	v_mfma_f32_16x16x32_bf16 v[134:137], v[170:173], v[202:205], v[134:137]
	v_subrev_u32_e32 v232, s61, v234
	v_ashrrev_i32_e32 v233, 31, v232
	v_lshl_add_u64 v[232:233], v[232:233], 1, s[4:5]
	v_mfma_f32_16x16x32_bf16 v[126:129], v[162:165], v[194:197], v[126:129]
	global_store_dwordx2 v[232:233], v[242:243], off nt
	s_add_i32 s22, s42, s47
	s_lshr_b32 s4, s22, 31
	v_mfma_f32_16x16x32_bf16 v[122:125], v[170:173], v[194:197], v[122:125]
	s_add_i32 s4, s22, s4
	s_ashr_i32 s23, s4, 1
	s_ashr_i32 s4, s4, 11
	v_mfma_f32_16x16x32_bf16 v[110:113], v[162:165], v[186:189], v[110:113]
	s_ashr_i32 s5, s4, 31
	s_lshl_b64 s[4:5], s[4:5], 25
	v_readlane_b32 s64, v251, 36
	v_mfma_f32_16x16x32_bf16 v[106:109], v[170:173], v[186:189], v[106:109]
	v_readlane_b32 s65, v251, 37
	s_add_u32 s4, s64, s4
	s_addc_u32 s5, s65, s5
	v_mfma_f32_16x16x32_bf16 v[94:97], v[162:165], v[178:181], v[94:97]
	s_lshl_b32 s64, s23, 15
	s_and_b32 s64, s64, 0x1ff8000
	s_add_u32 s64, s4, s64
	s_addc_u32 s65, s5, 0
	v_mfma_f32_16x16x32_bf16 v[90:93], v[170:173], v[178:181], v[90:93]
	s_setprio 0
	s_setprio 1
	s_lshl_b32 s4, s23, 12
	s_lshl_b32 s5, s22, 11
	s_sub_i32 s4, s5, s4
	v_mfma_f32_16x16x32_bf16 v[130:133], v[142:145], v[198:201], v[130:133]
	s_ashr_i32 s5, s4, 31
	s_lshl_b64 s[4:5], s[4:5], 2
	s_add_u32 s4, s64, s4
	s_addc_u32 s5, s65, s5
	v_mfma_f32_16x16x32_bf16 v[118:121], v[150:153], v[198:201], v[118:121]
	v_lshlrev_b32_e32 v2, 2, v208
	v_lshl_add_u64 v[232:233], s[4:5], 0, v[2:3]
	v_lshl_add_u64 v[232:233], v[232:233], 0, s[8:9]
	v_mfma_f32_16x16x32_bf16 v[114:117], v[142:145], v[190:193], v[114:117]
	global_load_dwordx4 v[242:245], v2, s[4:5] nt
	global_load_dwordx4 v[246:249], v[232:233], off nt
	s_mov_b32 s100, 3
	v_mfma_f32_16x16x32_bf16 v[102:105], v[150:153], v[190:193], v[102:105]
	s_mov_b32 s99, s42
	s_add_i32 s42, s42, 1
	v_mfma_f32_16x16x32_bf16 v[98:101], v[142:145], v[182:185], v[98:101]
	v_mfma_f32_16x16x32_bf16 v[86:89], v[150:153], v[182:185], v[86:89]
	v_mfma_f32_16x16x32_bf16 v[82:85], v[142:145], v[174:177], v[82:85]
	v_mfma_f32_16x16x32_bf16 v[78:81], v[150:153], v[174:177], v[78:81]
	v_mfma_f32_16x16x32_bf16 v[130:133], v[146:149], v[202:205], v[130:133]
	v_mfma_f32_16x16x32_bf16 v[118:121], v[154:157], v[202:205], v[118:121]
	v_mfma_f32_16x16x32_bf16 v[114:117], v[146:149], v[194:197], v[114:117]
	v_mfma_f32_16x16x32_bf16 v[102:105], v[154:157], v[194:197], v[102:105]
	v_mfma_f32_16x16x32_bf16 v[98:101], v[146:149], v[186:189], v[98:101]
	v_mfma_f32_16x16x32_bf16 v[86:89], v[154:157], v[186:189], v[86:89]
	v_mfma_f32_16x16x32_bf16 v[82:85], v[146:149], v[178:181], v[82:85]
	v_mfma_f32_16x16x32_bf16 v[78:81], v[154:157], v[178:181], v[78:81]
	s_setprio 0
	s_branch .Lp4vg_mmafter_b

; #define PG8_LAS __attribute__((address_space(3)))
;     __device__ __forceinline__ void issue(PG8_LAS unsigned char* lds0, int j, int tid, int wid) const {
;         const float* s0; unsigned char* d; addr(j, tid, s0, d);
;         __builtin_amdgcn_global_load_lds((const unsigned*)s0, (PG8_LAS unsigned*)(lds0 + stage + wid * 1024), 16, 0, 2);
;         __builtin_amdgcn_global_load_lds((const unsigned*)(s0 + ntot), (PG8_LAS unsigned*)(lds0 + stage + 8192 + wid * 1024), 16, 0, 2);
;     }
;     __device__ __forceinline__ void read(v4i_t& t0, v4i_t& t1, int tid, unsigned ldsb) const {
;         asm volatile("ds_read_b128 %0, %1" : "=&v"(t0) : "v"(ldsb + stage + 16u * (unsigned)tid) : "memory");
;         asm volatile("ds_read_b128 %0, %1" : "=&v"(t1) : "v"(ldsb + stage + 8192u + 16u * (unsigned)tid) : "memory");
;     }
;     __device__ __forceinline__ void finish(v4i_t& t0, v4i_t& t1, int j, int tid) const {
;         asm volatile("" : "+v"(t0), "+v"(t1));
;         const float* s0; unsigned char* d; addr(j, tid, s0, d);
;         const f32x4 r0 = __builtin_bit_cast(f32x4, t0) * 64.f, r1 = __builtin_bit_cast(f32x4, t1) * 64.f;
;         int w0 = 0, w1 = 0; w0 = __builtin_amdgcn_cvt_pk_fp8_f32(r0[0], r1[0], w0, false); w0 = __builtin_amdgcn_cvt_pk_fp8_f32(r0[1], r1[1], w0, true);
;         w1 = __builtin_amdgcn_cvt_pk_fp8_f32(r0[2], r1[2], w1, false); w1 = __builtin_amdgcn_cvt_pk_fp8_f32(r0[3], r1[3], w1, true);
;         typedef int v2is __attribute__((ext_vector_type(2))); __builtin_nontemporal_store((v2is){w0, w1}, (v2is*)d);
.Lp7vg_wd_a1:
	s_waitcnt lgkmcnt(0)
	s_cmp_lt_i32 s98, 0
	s_cbranch_scc1 .Lp7vg_mmslow_aB
	s_cmpk_gt_i32 s48, 0x7f
	s_cbranch_scc1 .Lp7vg_mmslow_aB
	s_barrier
	s_setprio 1
	v_mfma_scale_f32_16x16x128_f8f6f4 v[202:205], v[26:33], v[58:65], v[202:205], v226, v226 op_sel_hi:[0,0,0]
	s_add_i32 s4, s98, s52
	s_add_i32 s4, s4, 1
	v_pk_mul_f32 v[70:71], v[70:71], s[14:15] op_sel_hi:[1,0]
	v_pk_mul_f32 v[72:73], v[72:73], s[14:15] op_sel_hi:[1,0]
	v_mfma_scale_f32_16x16x128_f8f6f4 v[198:201], v[18:25], v[58:65], v[198:201], v226, v226 op_sel_hi:[0,0,0]
	v_pk_mul_f32 v[74:75], v[74:75], s[14:15] op_sel_hi:[1,0]
	v_pk_mul_f32 v[76:77], v[76:77], s[14:15] op_sel_hi:[1,0]
	s_ashr_i32 s2, s4, 10
	s_ashr_i32 s3, s2, 31
	v_mfma_scale_f32_16x16x128_f8f6f4 v[186:189], v[26:33], v[50:57], v[186:189], v226, v226 op_sel_hi:[0,0,0]
	v_cvt_pk_fp8_f32 v70, v70, v74
	s_lshl_b32 s4, s4, 12
	s_lshl_b64 s[2:3], s[2:3], 22
	v_cvt_pk_fp8_f32 v70, v71, v75 op_sel:[0,0,1]
	v_mfma_scale_f32_16x16x128_f8f6f4 v[182:185], v[18:25], v[50:57], v[182:185], v226, v226 op_sel_hi:[0,0,0]
	s_and_b32 s4, s4, 0x3ff000
	v_readlane_b32 s5, v251, 50
	v_cvt_pk_fp8_f32 v71, v72, v76
	s_add_u32 s2, s5, s2
	v_mfma_scale_f32_16x16x128_f8f6f4 v[170:173], v[26:33], v[42:49], v[170:173], v226, v226 op_sel_hi:[0,0,0]
	v_readlane_b32 s5, v251, 51
	s_addc_u32 s3, s5, s3
	v_cvt_pk_fp8_f32 v71, v73, v77 op_sel:[0,0,1]
	s_add_u32 s2, s2, s4
	s_addc_u32 s3, s3, 0
	v_mfma_scale_f32_16x16x128_f8f6f4 v[166:169], v[18:25], v[42:49], v[166:169], v226, v226 op_sel_hi:[0,0,0]
	v_lshl_add_u64 v[68:69], s[2:3], 0, v[210:211]
	global_store_dwordx2 v[68:69], v[70:71], off nt
	s_add_i32 s4, s48, s53
	s_ashr_i32 s2, s4, 10
	v_mfma_scale_f32_16x16x128_f8f6f4 v[154:157], v[26:33], v[34:41], v[154:157], v226, v226 op_sel_hi:[0,0,0]
	s_ashr_i32 s3, s2, 31
	s_lshl_b64 s[2:3], s[2:3], 24
	s_lshl_b32 s4, s4, 14
	s_and_b32 s4, s4, 0xffc000
	v_mfma_scale_f32_16x16x128_f8f6f4 v[150:153], v[18:25], v[34:41], v[150:153], v226, v226 op_sel_hi:[0,0,0]
	s_setprio 0
	s_setprio 1
	s_add_u32 s2, s76, s2
	s_addc_u32 s3, s77, s3
	s_add_u32 s2, s2, s4
	s_addc_u32 s3, s3, 0
	v_mfma_scale_f32_16x16x128_f8f6f4 v[194:197], v[10:17], v[58:65], v[194:197], v226, v226 op_sel_hi:[0,0,0]
	v_lshlrev_b32_e32 v66, 2, v208
	v_lshl_add_u64 v[68:69], s[2:3], 0, v[66:67]
	v_lshl_add_u64 v[68:69], v[68:69], 0, s[16:17]
	global_load_dwordx4 v[70:73], v66, s[2:3] nt
	v_mfma_scale_f32_16x16x128_f8f6f4 v[190:193], v[2:9], v[58:65], v[190:193], v226, v226 op_sel_hi:[0,0,0]
	global_load_dwordx4 v[74:77], v[68:69], off nt
	s_mov_b32 s100, 3
	s_mov_b32 s98, s48
	s_add_i32 s48, s48, 1
	v_mfma_scale_f32_16x16x128_f8f6f4 v[178:181], v[10:17], v[50:57], v[178:181], v226, v226 op_sel_hi:[0,0,0]
	s_add_u32 s2, s42, 0xfffc0080
	s_addc_u32 s3, s43, -1
	s_cmp_eq_u32 s64, 12
	s_cselect_b32 s5, s23, s3
	s_cselect_b32 s4, s25, s2
	s_cselect_b32 s45, s35, s63
	s_cselect_b32 s44, s61, s62
	v_mfma_scale_f32_16x16x128_f8f6f4 v[174:177], v[2:9], v[50:57], v[174:177], v226, v226 op_sel_hi:[0,0,0]
	v_mfma_scale_f32_16x16x128_f8f6f4 v[162:165], v[10:17], v[42:49], v[162:165], v226, v226 op_sel_hi:[0,0,0]
	v_mfma_scale_f32_16x16x128_f8f6f4 v[158:161], v[2:9], v[42:49], v[158:161], v226, v226 op_sel_hi:[0,0,0]
	v_mfma_scale_f32_16x16x128_f8f6f4 v[146:149], v[10:17], v[34:41], v[146:149], v226, v226 op_sel_hi:[0,0,0]
	v_mfma_scale_f32_16x16x128_f8f6f4 v[142:145], v[2:9], v[34:41], v[142:145], v226, v226 op_sel_hi:[0,0,0]
	s_setprio 0
	s_branch .Lp7vg_mmjoin_a
.Lp7vg_mmslow_aB:
	s_barrier
.Lp7vg_mmslow_a:
	s_mov_b32 s100, 0
	s_cmp_lt_i32 s98, 0
	s_cbranch_scc1 .Lp7vg_nf_a
	s_add_i32 s4, s98, s52
	s_add_i32 s4, s4, 1
	v_pk_mul_f32 v[70:71], v[70:71], s[14:15] op_sel_hi:[1,0]
	v_pk_mul_f32 v[72:73], v[72:73], s[14:15] op_sel_hi:[1,0]
	v_pk_mul_f32 v[74:75], v[74:75], s[14:15] op_sel_hi:[1,0]
	v_pk_mul_f32 v[76:77], v[76:77], s[14:15] op_sel_hi:[1,0]
	s_ashr_i32 s2, s4, 10
	s_ashr_i32 s3, s2, 31
	v_cvt_pk_fp8_f32 v70, v70, v74
	s_lshl_b32 s4, s4, 12
	s_lshl_b64 s[2:3], s[2:3], 22
	v_cvt_pk_fp8_f32 v70, v71, v75 op_sel:[0,0,1]
	s_and_b32 s4, s4, 0x3ff000
	v_readlane_b32 s5, v251, 50
	v_cvt_pk_fp8_f32 v71, v72, v76
	s_add_u32 s2, s5, s2
	v_readlane_b32 s5, v251, 51
	s_addc_u32 s3, s5, s3
	v_cvt_pk_fp8_f32 v71, v73, v77 op_sel:[0,0,1]
	s_add_u32 s2, s2, s4
	s_addc_u32 s3, s3, 0
	v_lshl_add_u64 v[68:69], s[2:3], 0, v[210:211]
	global_store_dwordx2 v[68:69], v[70:71], off nt
	s_mov_b32 s100, 1

.Lp7dma_wd_a:
	s_waitcnt lgkmcnt(0)
	s_cbranch_vccnz .Lp7dma_skip_bB
	s_barrier
	s_setprio 1
	v_mfma_scale_f32_16x16x128_f8f6f4 v[138:141], v[26:33], v[58:65], v[138:141], v226, v226 op_sel_hi:[0,0,0]
	v_mfma_scale_f32_16x16x128_f8f6f4 v[134:137], v[18:25], v[58:65], v[134:137], v226, v226 op_sel_hi:[0,0,0]
	v_mfma_scale_f32_16x16x128_f8f6f4 v[122:125], v[26:33], v[50:57], v[122:125], v226, v226 op_sel_hi:[0,0,0]
	v_mfma_scale_f32_16x16x128_f8f6f4 v[118:121], v[18:25], v[50:57], v[118:121], v226, v226 op_sel_hi:[0,0,0]
	v_mfma_scale_f32_16x16x128_f8f6f4 v[106:109], v[26:33], v[42:49], v[106:109], v226, v226 op_sel_hi:[0,0,0]
	v_mfma_scale_f32_16x16x128_f8f6f4 v[102:105], v[18:25], v[42:49], v[102:105], v226, v226 op_sel_hi:[0,0,0]
	v_mfma_scale_f32_16x16x128_f8f6f4 v[90:93], v[26:33], v[34:41], v[90:93], v226, v226 op_sel_hi:[0,0,0]
	v_mfma_scale_f32_16x16x128_f8f6f4 v[86:89], v[18:25], v[34:41], v[86:89], v226, v226 op_sel_hi:[0,0,0]
	s_setprio 0
	s_setprio 1
	v_mfma_scale_f32_16x16x128_f8f6f4 v[130:133], v[10:17], v[58:65], v[130:133], v226, v226 op_sel_hi:[0,0,0]
	v_mfma_scale_f32_16x16x128_f8f6f4 v[126:129], v[2:9], v[58:65], v[126:129], v226, v226 op_sel_hi:[0,0,0]
	v_mfma_scale_f32_16x16x128_f8f6f4 v[114:117], v[10:17], v[50:57], v[114:117], v226, v226 op_sel_hi:[0,0,0]
	v_lshl_add_u64 v[68:69], s[4:5], 0, v[212:213]
	s_mov_b32 m0, s15
	v_cmp_ne_u32_e64 s[2:3], 1, v66
	global_load_lds_dwordx4 v[68:69], off
	v_mfma_scale_f32_16x16x128_f8f6f4 v[110:113], v[2:9], v[50:57], v[110:113], v226, v226 op_sel_hi:[0,0,0]
	v_mfma_scale_f32_16x16x128_f8f6f4 v[98:101], v[10:17], v[42:49], v[98:101], v226, v226 op_sel_hi:[0,0,0]
	s_mov_b32 m0, s49
	s_nop 0
	global_load_lds_dwordx4 v[224:225], off
	v_mfma_scale_f32_16x16x128_f8f6f4 v[94:97], v[2:9], v[42:49], v[94:97], v226, v226 op_sel_hi:[0,0,0]
	v_mfma_scale_f32_16x16x128_f8f6f4 v[82:85], v[10:17], v[34:41], v[82:85], v226, v226 op_sel_hi:[0,0,0]
	v_mfma_scale_f32_16x16x128_f8f6f4 v[78:81], v[2:9], v[34:41], v[78:81], v226, v226 op_sel_hi:[0,0,0]
	s_setprio 0

; #define PG8_LAS __attribute__((address_space(3)))
;     __device__ __forceinline__ void issue(PG8_LAS unsigned char* lds0, int j, int tid, int wid) const {
;         const float* s0; unsigned char* d; addr(j, tid, s0, d);
;         __builtin_amdgcn_global_load_lds((const unsigned*)s0, (PG8_LAS unsigned*)(lds0 + stage + wid * 1024), 16, 0, 2);
;         __builtin_amdgcn_global_load_lds((const unsigned*)(s0 + ntot), (PG8_LAS unsigned*)(lds0 + stage + 8192 + wid * 1024), 16, 0, 2);
;     }
;     __device__ __forceinline__ void read(v4i_t& t0, v4i_t& t1, int tid, unsigned ldsb) const {
;         asm volatile("ds_read_b128 %0, %1" : "=&v"(t0) : "v"(ldsb + stage + 16u * (unsigned)tid) : "memory");
;         asm volatile("ds_read_b128 %0, %1" : "=&v"(t1) : "v"(ldsb + stage + 8192u + 16u * (unsigned)tid) : "memory");
;     }
;     __device__ __forceinline__ void finish(v4i_t& t0, v4i_t& t1, int j, int tid) const {
;         asm volatile("" : "+v"(t0), "+v"(t1));
;         const float* s0; unsigned char* d; addr(j, tid, s0, d);
;         const f32x4 r0 = __builtin_bit_cast(f32x4, t0) * 64.f, r1 = __builtin_bit_cast(f32x4, t1) * 64.f;
;         int w0 = 0, w1 = 0; w0 = __builtin_amdgcn_cvt_pk_fp8_f32(r0[0], r1[0], w0, false); w0 = __builtin_amdgcn_cvt_pk_fp8_f32(r0[1], r1[1], w0, true);
;         w1 = __builtin_amdgcn_cvt_pk_fp8_f32(r0[2], r1[2], w1, false); w1 = __builtin_amdgcn_cvt_pk_fp8_f32(r0[3], r1[3], w1, true);
;         typedef int v2is __attribute__((ext_vector_type(2))); __builtin_nontemporal_store((v2is){w0, w1}, (v2is*)d);
.Lp7vg_wd_b1:
	s_waitcnt lgkmcnt(0)
	s_cmp_lt_i32 s99, 0
	s_cbranch_scc1 .Lp7vg_mmslow_bB
	s_cmpk_gt_i32 s48, 0x7f
	s_cbranch_scc1 .Lp7vg_mmslow_bB
	s_barrier
	s_setprio 1
	v_mfma_scale_f32_16x16x128_f8f6f4 v[202:205], v[26:33], v[58:65], v[202:205], v226, v226 op_sel_hi:[0,0,0]
	s_add_i32 s65, s99, s52
	s_add_i32 s65, s65, 1
	v_pk_mul_f32 v[242:243], v[242:243], s[14:15] op_sel_hi:[1,0]
	v_pk_mul_f32 v[244:245], v[244:245], s[14:15] op_sel_hi:[1,0]
	v_mfma_scale_f32_16x16x128_f8f6f4 v[198:201], v[18:25], v[58:65], v[198:201], v226, v226 op_sel_hi:[0,0,0]
	v_pk_mul_f32 v[246:247], v[246:247], s[14:15] op_sel_hi:[1,0]
	v_pk_mul_f32 v[248:249], v[248:249], s[14:15] op_sel_hi:[1,0]
	s_ashr_i32 s46, s65, 10
	s_ashr_i32 s47, s46, 31
	v_mfma_scale_f32_16x16x128_f8f6f4 v[186:189], v[26:33], v[50:57], v[186:189], v226, v226 op_sel_hi:[0,0,0]
	v_cvt_pk_fp8_f32 v242, v242, v246
	s_lshl_b32 s65, s65, 12
	s_lshl_b64 s[46:47], s[46:47], 22
	v_cvt_pk_fp8_f32 v242, v243, v247 op_sel:[0,0,1]
	v_mfma_scale_f32_16x16x128_f8f6f4 v[182:185], v[18:25], v[50:57], v[182:185], v226, v226 op_sel_hi:[0,0,0]
	s_and_b32 s65, s65, 0x3ff000
	v_readlane_b32 s4, v251, 50
	v_cvt_pk_fp8_f32 v243, v244, v248
	s_add_u32 s46, s4, s46
	v_mfma_scale_f32_16x16x128_f8f6f4 v[170:173], v[26:33], v[42:49], v[170:173], v226, v226 op_sel_hi:[0,0,0]
	v_readlane_b32 s4, v251, 51
	s_addc_u32 s47, s4, s47
	v_cvt_pk_fp8_f32 v243, v245, v249 op_sel:[0,0,1]
	s_add_u32 s46, s46, s65
	s_addc_u32 s47, s47, 0
	v_mfma_scale_f32_16x16x128_f8f6f4 v[166:169], v[18:25], v[42:49], v[166:169], v226, v226 op_sel_hi:[0,0,0]
	v_lshl_add_u64 v[240:241], s[46:47], 0, v[210:211]
	global_store_dwordx2 v[240:241], v[242:243], off nt
	s_add_i32 s65, s48, s53
	s_ashr_i32 s46, s65, 10
	v_mfma_scale_f32_16x16x128_f8f6f4 v[154:157], v[26:33], v[34:41], v[154:157], v226, v226 op_sel_hi:[0,0,0]
	s_ashr_i32 s47, s46, 31
	s_lshl_b64 s[46:47], s[46:47], 24
	s_lshl_b32 s65, s65, 14
	s_and_b32 s65, s65, 0xffc000
	v_mfma_scale_f32_16x16x128_f8f6f4 v[150:153], v[18:25], v[34:41], v[150:153], v226, v226 op_sel_hi:[0,0,0]
	s_setprio 0
	s_setprio 1
	s_add_u32 s46, s76, s46
	s_addc_u32 s47, s77, s47
	s_add_u32 s46, s46, s65
	s_addc_u32 s47, s47, 0
	v_mfma_scale_f32_16x16x128_f8f6f4 v[194:197], v[10:17], v[58:65], v[194:197], v226, v226 op_sel_hi:[0,0,0]
	v_lshlrev_b32_e32 v66, 2, v208
	v_lshl_add_u64 v[240:241], s[46:47], 0, v[66:67]
	v_lshl_add_u64 v[240:241], v[240:241], 0, s[16:17]
	global_load_dwordx4 v[242:245], v66, s[46:47] nt
	v_mfma_scale_f32_16x16x128_f8f6f4 v[190:193], v[2:9], v[58:65], v[190:193], v226, v226 op_sel_hi:[0,0,0]
	global_load_dwordx4 v[246:249], v[240:241], off nt
	s_mov_b32 s100, 3
	s_mov_b32 s99, s48
	s_add_i32 s48, s48, 1
	v_mfma_scale_f32_16x16x128_f8f6f4 v[178:181], v[10:17], v[50:57], v[178:181], v226, v226 op_sel_hi:[0,0,0]
	s_add_u32 s46, s44, 0x84000
	s_addc_u32 s47, s45, 0
	v_mfma_scale_f32_16x16x128_f8f6f4 v[174:177], v[2:9], v[50:57], v[174:177], v226, v226 op_sel_hi:[0,0,0]
	v_mfma_scale_f32_16x16x128_f8f6f4 v[162:165], v[10:17], v[42:49], v[162:165], v226, v226 op_sel_hi:[0,0,0]
	v_mfma_scale_f32_16x16x128_f8f6f4 v[158:161], v[2:9], v[42:49], v[158:161], v226, v226 op_sel_hi:[0,0,0]
	v_mfma_scale_f32_16x16x128_f8f6f4 v[146:149], v[10:17], v[34:41], v[146:149], v226, v226 op_sel_hi:[0,0,0]
	v_mfma_scale_f32_16x16x128_f8f6f4 v[142:145], v[2:9], v[34:41], v[142:145], v226, v226 op_sel_hi:[0,0,0]
	s_setprio 0
	s_branch .Lp7vg_mmjoin_b
.Lp7vg_mmslow_bB:
	s_barrier
.Lp7vg_mmslow_b:
	s_mov_b32 s100, 0
	s_cmp_lt_i32 s99, 0
	s_cbranch_scc1 .Lp7vg_nf_b
	s_add_i32 s65, s99, s52
	s_add_i32 s65, s65, 1
	v_pk_mul_f32 v[242:243], v[242:243], s[14:15] op_sel_hi:[1,0]
	v_pk_mul_f32 v[244:245], v[244:245], s[14:15] op_sel_hi:[1,0]
	v_pk_mul_f32 v[246:247], v[246:247], s[14:15] op_sel_hi:[1,0]
	v_pk_mul_f32 v[248:249], v[248:249], s[14:15] op_sel_hi:[1,0]
	s_ashr_i32 s46, s65, 10
	s_ashr_i32 s47, s46, 31
	v_cvt_pk_fp8_f32 v242, v242, v246
	s_lshl_b32 s65, s65, 12
	s_lshl_b64 s[46:47], s[46:47], 22
	v_cvt_pk_fp8_f32 v242, v243, v247 op_sel:[0,0,1]
	s_and_b32 s65, s65, 0x3ff000
	v_readlane_b32 s4, v251, 50
	v_cvt_pk_fp8_f32 v243, v244, v248
	s_add_u32 s46, s4, s46
	v_readlane_b32 s4, v251, 51
	s_addc_u32 s47, s4, s47
	v_cvt_pk_fp8_f32 v243, v245, v249 op_sel:[0,0,1]
	s_add_u32 s46, s46, s65
	s_addc_u32 s47, s47, 0
	v_lshl_add_u64 v[240:241], s[46:47], 0, v[210:211]
	global_store_dwordx2 v[240:241], v[242:243], off nt
	s_mov_b32 s100, 1

.Lp7dma_wd_b:
	s_waitcnt lgkmcnt(0)
	s_cbranch_vccnz .Lp7dma_skip_dB
	s_barrier
	s_setprio 1
	v_mfma_scale_f32_16x16x128_f8f6f4 v[138:141], v[26:33], v[58:65], v[138:141], v226, v226 op_sel_hi:[0,0,0]
	v_mfma_scale_f32_16x16x128_f8f6f4 v[134:137], v[18:25], v[58:65], v[134:137], v226, v226 op_sel_hi:[0,0,0]
	v_mfma_scale_f32_16x16x128_f8f6f4 v[122:125], v[26:33], v[50:57], v[122:125], v226, v226 op_sel_hi:[0,0,0]
	v_mfma_scale_f32_16x16x128_f8f6f4 v[118:121], v[18:25], v[50:57], v[118:121], v226, v226 op_sel_hi:[0,0,0]
	v_mfma_scale_f32_16x16x128_f8f6f4 v[106:109], v[26:33], v[42:49], v[106:109], v226, v226 op_sel_hi:[0,0,0]
	v_mfma_scale_f32_16x16x128_f8f6f4 v[102:105], v[18:25], v[42:49], v[102:105], v226, v226 op_sel_hi:[0,0,0]
	v_mfma_scale_f32_16x16x128_f8f6f4 v[90:93], v[26:33], v[34:41], v[90:93], v226, v226 op_sel_hi:[0,0,0]
	v_mfma_scale_f32_16x16x128_f8f6f4 v[86:89], v[18:25], v[34:41], v[86:89], v226, v226 op_sel_hi:[0,0,0]
	s_setprio 0
	s_setprio 1
	v_mfma_scale_f32_16x16x128_f8f6f4 v[130:133], v[10:17], v[58:65], v[130:133], v226, v226 op_sel_hi:[0,0,0]
	v_mfma_scale_f32_16x16x128_f8f6f4 v[126:129], v[2:9], v[58:65], v[126:129], v226, v226 op_sel_hi:[0,0,0]
	v_mfma_scale_f32_16x16x128_f8f6f4 v[114:117], v[10:17], v[50:57], v[114:117], v226, v226 op_sel_hi:[0,0,0]
	s_mov_b32 m0, s54
	s_nop 0
	global_load_lds_dwordx4 v[68:69], off
	v_mfma_scale_f32_16x16x128_f8f6f4 v[110:113], v[2:9], v[50:57], v[110:113], v226, v226 op_sel_hi:[0,0,0]
	v_mfma_scale_f32_16x16x128_f8f6f4 v[98:101], v[10:17], v[42:49], v[98:101], v226, v226 op_sel_hi:[0,0,0]
	v_lshl_add_u64 v[68:69], v[224:225], 0, s[10:11]
	s_mov_b32 m0, s55
	s_nop 0
	global_load_lds_dwordx4 v[68:69], off
	v_mfma_scale_f32_16x16x128_f8f6f4 v[94:97], v[2:9], v[42:49], v[94:97], v226, v226 op_sel_hi:[0,0,0]
	v_mfma_scale_f32_16x16x128_f8f6f4 v[82:85], v[10:17], v[34:41], v[82:85], v226, v226 op_sel_hi:[0,0,0]
	v_mfma_scale_f32_16x16x128_f8f6f4 v[78:81], v[2:9], v[34:41], v[78:81], v226, v226 op_sel_hi:[0,0,0]
	s_setprio 0
	s_branch .LBB0_781
.Lp7dma_skip_bB:
	s_barrier
.Lp7dma_skip_b:
	v_lshl_add_u64 v[68:69], s[4:5], 0, v[212:213]
	s_mov_b32 m0, s15
	v_cmp_ne_u32_e64 s[2:3], 1, v66
	global_load_lds_dwordx4 v[68:69], off
	s_mov_b32 m0, s49
	s_nop 0
	global_load_lds_dwordx4 v[224:225], off
	s_branch .LBB0_790
.Lp7dma_skip_dB:
	s_barrier
.Lp7dma_skip_d:
	s_mov_b32 m0, s54
	s_nop 0
	global_load_lds_dwordx4 v[68:69], off
	v_lshl_add_u64 v[68:69], v[224:225], 0, s[10:11]
	s_mov_b32 m0, s55
	s_nop 0
	global_load_lds_dwordx4 v[68:69], off
	s_branch .LBB0_781

.LBB0_901:
	ds_read_b64_tr_b16 v[26:27], v207 offset:0
	ds_read_b64_tr_b16 v[28:29], v207 offset:1024
	ds_read_b64_tr_b16 v[30:31], v207 offset:8192
	ds_read_b64_tr_b16 v[32:33], v207 offset:9216
	ds_read_b64_tr_b16 v[18:19], v217 offset:0
	ds_read_b64_tr_b16 v[20:21], v217 offset:1024
	ds_read_b64_tr_b16 v[22:23], v217 offset:8192
	ds_read_b64_tr_b16 v[24:25], v217 offset:9216
	ds_read_b64_tr_b16 v[10:11], v214 offset:0
	ds_read_b64_tr_b16 v[12:13], v214 offset:1024
	ds_read_b64_tr_b16 v[14:15], v214 offset:8192
	ds_read_b64_tr_b16 v[16:17], v214 offset:9216
	ds_read_b64_tr_b16 v[2:3], v218 offset:0
	ds_read_b64_tr_b16 v[4:5], v218 offset:1024
	ds_read_b64_tr_b16 v[6:7], v218 offset:8192
	ds_read_b64_tr_b16 v[8:9], v218 offset:9216
	s_add_u32 s2, s50, 0xfffc0080
	s_addc_u32 s3, s51, -1
	s_cmp_eq_u32 s72, 12
	s_cselect_b32 s55, s29, s3
	s_cselect_b32 s54, s31, s2
	s_cselect_b32 s53, s35, s71
	s_cselect_b32 s52, s43, s70
	ds_read_b128 v[34:37], v223
	ds_read_b128 v[38:41], v223 offset:1024
	ds_read_b128 v[42:45], v223 offset:2048
	ds_read_b128 v[46:49], v223 offset:3072
	ds_read_b128 v[50:53], v223 offset:4096
	ds_read_b128 v[54:57], v223 offset:5120
	ds_read_b128 v[58:61], v223 offset:6144
	ds_read_b128 v[62:65], v223 offset:7168
	s_waitcnt vmcnt(6)
	s_waitcnt lgkmcnt(0)
	s_barrier
	s_setprio 1
	v_mfma_scale_f32_16x16x128_f8f6f4 v[194:197], v[26:33], v[34:41], v[194:197], v1, v1 op_sel_hi:[0,0,0]
	v_mfma_scale_f32_16x16x128_f8f6f4 v[190:193], v[18:25], v[34:41], v[190:193], v1, v1 op_sel_hi:[0,0,0]
	v_mfma_scale_f32_16x16x128_f8f6f4 v[186:189], v[26:33], v[42:49], v[186:189], v1, v1 op_sel_hi:[0,0,0]
	v_mfma_scale_f32_16x16x128_f8f6f4 v[182:185], v[18:25], v[42:49], v[182:185], v1, v1 op_sel_hi:[0,0,0]
	v_lshl_add_u64 v[68:69], s[50:51], 0, v[208:209]
	s_add_i32 m0, s17, 0xc000
	s_nop 0
	global_load_lds_dwordx4 v[68:69], off
	v_mfma_scale_f32_16x16x128_f8f6f4 v[162:165], v[26:33], v[50:57], v[162:165], v1, v1 op_sel_hi:[0,0,0]
	v_mfma_scale_f32_16x16x128_f8f6f4 v[158:161], v[18:25], v[50:57], v[158:161], v1, v1 op_sel_hi:[0,0,0]
	v_mfma_scale_f32_16x16x128_f8f6f4 v[146:149], v[26:33], v[58:65], v[146:149], v1, v1 op_sel_hi:[0,0,0]
	v_mfma_scale_f32_16x16x128_f8f6f4 v[142:145], v[18:25], v[58:65], v[142:145], v1, v1 op_sel_hi:[0,0,0]
	s_setprio 0
	s_setprio 1
	v_mfma_scale_f32_16x16x128_f8f6f4 v[178:181], v[10:17], v[34:41], v[178:181], v1, v1 op_sel_hi:[0,0,0]
	v_mfma_scale_f32_16x16x128_f8f6f4 v[174:177], v[2:9], v[34:41], v[174:177], v1, v1 op_sel_hi:[0,0,0]
	v_lshl_add_u64 v[68:69], s[50:51], 0, v[210:211]
	s_add_i32 m0, s17, 0xe000
	s_nop 0
	global_load_lds_dwordx4 v[68:69], off
	v_mfma_scale_f32_16x16x128_f8f6f4 v[170:173], v[10:17], v[42:49], v[170:173], v1, v1 op_sel_hi:[0,0,0]
	v_mfma_scale_f32_16x16x128_f8f6f4 v[166:169], v[2:9], v[42:49], v[166:169], v1, v1 op_sel_hi:[0,0,0]
	v_mfma_scale_f32_16x16x128_f8f6f4 v[154:157], v[10:17], v[50:57], v[154:157], v1, v1 op_sel_hi:[0,0,0]
	v_mfma_scale_f32_16x16x128_f8f6f4 v[150:153], v[2:9], v[50:57], v[150:153], v1, v1 op_sel_hi:[0,0,0]
	v_mfma_scale_f32_16x16x128_f8f6f4 v[138:141], v[10:17], v[58:65], v[138:141], v1, v1 op_sel_hi:[0,0,0]
	v_mfma_scale_f32_16x16x128_f8f6f4 v[134:137], v[2:9], v[58:65], v[134:137], v1, v1 op_sel_hi:[0,0,0]
	s_setprio 0
	s_barrier
	s_mov_b32 m0, s19
	v_lshl_add_u64 v[68:69], s[52:53], 0, v[200:201]
	global_load_lds_dwordx4 v[68:69], off
	v_lshl_add_u64 v[212:213], s[52:53], 0, v[204:205]
	s_mov_b32 m0, s33
	v_lshl_add_u64 v[68:69], v[68:69], 0, s[4:5]
	global_load_lds_dwordx4 v[212:213], off
	s_mov_b32 m0, s45
	s_nop 0
	global_load_lds_dwordx4 v[68:69], off
	v_lshl_add_u64 v[68:69], v[212:213], 0, s[4:5]
	s_mov_b32 m0, s47
	v_lshl_add_u64 v[212:213], s[54:55], 0, v[202:203]
	global_load_lds_dwordx4 v[68:69], off
	s_andn2_b64 vcc, exec, s[48:49]
	s_cbranch_vccnz .Lhalfskip_p8a
	ds_read_b128 v[58:61], v223 offset:16384
	ds_read_b128 v[62:65], v223 offset:17408
	ds_read_b128 v[50:53], v223 offset:18432
	ds_read_b128 v[54:57], v223 offset:19456
	ds_read_b128 v[42:45], v223 offset:20480
	ds_read_b128 v[46:49], v223 offset:21504
	ds_read_b128 v[34:37], v223 offset:22528
	ds_read_b128 v[38:41], v223 offset:23552
.Lhalfskip_p8a:
	v_cmp_ne_u32_e64 s[2:3], 1, v225
	s_waitcnt vmcnt(6)
	s_waitcnt lgkmcnt(0)
	s_cbranch_vccnz .Lp8_skip_bB
	s_barrier
	s_setprio 1
	v_mfma_scale_f32_16x16x128_f8f6f4 v[130:133], v[26:33], v[58:65], v[130:133], v1, v1 op_sel_hi:[0,0,0]
	v_mfma_scale_f32_16x16x128_f8f6f4 v[126:129], v[18:25], v[58:65], v[126:129], v1, v1 op_sel_hi:[0,0,0]
	v_mfma_scale_f32_16x16x128_f8f6f4 v[114:117], v[26:33], v[50:57], v[114:117], v1, v1 op_sel_hi:[0,0,0]
	v_mfma_scale_f32_16x16x128_f8f6f4 v[110:113], v[18:25], v[50:57], v[110:113], v1, v1 op_sel_hi:[0,0,0]
	v_mfma_scale_f32_16x16x128_f8f6f4 v[98:101], v[26:33], v[42:49], v[98:101], v1, v1 op_sel_hi:[0,0,0]
	v_mfma_scale_f32_16x16x128_f8f6f4 v[94:97], v[18:25], v[42:49], v[94:97], v1, v1 op_sel_hi:[0,0,0]
	v_mfma_scale_f32_16x16x128_f8f6f4 v[82:85], v[26:33], v[34:41], v[82:85], v1, v1 op_sel_hi:[0,0,0]
	v_mfma_scale_f32_16x16x128_f8f6f4 v[78:81], v[18:25], v[34:41], v[78:81], v1, v1 op_sel_hi:[0,0,0]
	s_setprio 0
	s_setprio 1
	v_mfma_scale_f32_16x16x128_f8f6f4 v[122:125], v[10:17], v[58:65], v[122:125], v1, v1 op_sel_hi:[0,0,0]
	v_mfma_scale_f32_16x16x128_f8f6f4 v[118:121], v[2:9], v[58:65], v[118:121], v1, v1 op_sel_hi:[0,0,0]
	v_mfma_scale_f32_16x16x128_f8f6f4 v[106:109], v[10:17], v[50:57], v[106:109], v1, v1 op_sel_hi:[0,0,0]
	v_lshl_add_u64 v[68:69], s[54:55], 0, v[198:199]
	s_mov_b32 m0, s17
	s_nop 0
	global_load_lds_dwordx4 v[68:69], off
	v_mfma_scale_f32_16x16x128_f8f6f4 v[102:105], v[2:9], v[50:57], v[102:105], v1, v1 op_sel_hi:[0,0,0]
	v_mfma_scale_f32_16x16x128_f8f6f4 v[90:93], v[10:17], v[42:49], v[90:93], v1, v1 op_sel_hi:[0,0,0]
	s_mov_b32 m0, s58
	s_nop 0
	global_load_lds_dwordx4 v[212:213], off
	v_mfma_scale_f32_16x16x128_f8f6f4 v[86:89], v[2:9], v[42:49], v[86:89], v1, v1 op_sel_hi:[0,0,0]
	v_mfma_scale_f32_16x16x128_f8f6f4 v[74:77], v[10:17], v[34:41], v[74:77], v1, v1 op_sel_hi:[0,0,0]
	v_mfma_scale_f32_16x16x128_f8f6f4 v[70:73], v[2:9], v[34:41], v[70:73], v1, v1 op_sel_hi:[0,0,0]
	s_setprio 0
.LBB0_903:
	s_add_u32 s56, s52, 0x40000
	s_addc_u32 s57, s53, 0
	s_barrier
	ds_read_b64_tr_b16 v[26:27], v215 offset:0
	ds_read_b64_tr_b16 v[28:29], v215 offset:1024
	ds_read_b64_tr_b16 v[30:31], v215 offset:8192
	ds_read_b64_tr_b16 v[32:33], v215 offset:9216
	ds_read_b64_tr_b16 v[18:19], v219 offset:0
	ds_read_b64_tr_b16 v[20:21], v219 offset:1024
	ds_read_b64_tr_b16 v[22:23], v219 offset:8192
	ds_read_b64_tr_b16 v[24:25], v219 offset:9216
	ds_read_b64_tr_b16 v[10:11], v216 offset:0
	ds_read_b64_tr_b16 v[12:13], v216 offset:1024
	ds_read_b64_tr_b16 v[14:15], v216 offset:8192
	ds_read_b64_tr_b16 v[16:17], v216 offset:9216
	ds_read_b64_tr_b16 v[2:3], v220 offset:0
	ds_read_b64_tr_b16 v[4:5], v220 offset:1024
	ds_read_b64_tr_b16 v[6:7], v220 offset:8192
	ds_read_b64_tr_b16 v[8:9], v220 offset:9216
	s_add_u32 s54, s54, 0x40000
	s_addc_u32 s55, s55, 0
	ds_read_b128 v[34:37], v223 offset:32768
	ds_read_b128 v[38:41], v223 offset:33792
	ds_read_b128 v[42:45], v223 offset:34816
	ds_read_b128 v[46:49], v223 offset:35840
	ds_read_b128 v[50:53], v223 offset:36864
	ds_read_b128 v[54:57], v223 offset:37888
	ds_read_b128 v[58:61], v223 offset:38912
	ds_read_b128 v[62:65], v223 offset:39936
	s_waitcnt vmcnt(6)
	s_waitcnt lgkmcnt(0)
	s_barrier
	s_setprio 1
	v_mfma_scale_f32_16x16x128_f8f6f4 v[194:197], v[26:33], v[34:41], v[194:197], v1, v1 op_sel_hi:[0,0,0]
	v_mfma_scale_f32_16x16x128_f8f6f4 v[190:193], v[18:25], v[34:41], v[190:193], v1, v1 op_sel_hi:[0,0,0]
	v_mfma_scale_f32_16x16x128_f8f6f4 v[186:189], v[26:33], v[42:49], v[186:189], v1, v1 op_sel_hi:[0,0,0]
	v_mfma_scale_f32_16x16x128_f8f6f4 v[182:185], v[18:25], v[42:49], v[182:185], v1, v1 op_sel_hi:[0,0,0]
	s_mov_b32 m0, s59
	v_lshl_add_u64 v[226:227], s[54:55], 0, v[198:199]
	global_load_lds_dwordx4 v[226:227], off
	v_mfma_scale_f32_16x16x128_f8f6f4 v[162:165], v[26:33], v[50:57], v[162:165], v1, v1 op_sel_hi:[0,0,0]
	v_mfma_scale_f32_16x16x128_f8f6f4 v[158:161], v[18:25], v[50:57], v[158:161], v1, v1 op_sel_hi:[0,0,0]
	v_mfma_scale_f32_16x16x128_f8f6f4 v[146:149], v[26:33], v[58:65], v[146:149], v1, v1 op_sel_hi:[0,0,0]
	v_mfma_scale_f32_16x16x128_f8f6f4 v[142:145], v[18:25], v[58:65], v[142:145], v1, v1 op_sel_hi:[0,0,0]
	s_setprio 0
	s_setprio 1
	v_mfma_scale_f32_16x16x128_f8f6f4 v[178:181], v[10:17], v[34:41], v[178:181], v1, v1 op_sel_hi:[0,0,0]
	v_mfma_scale_f32_16x16x128_f8f6f4 v[174:177], v[2:9], v[34:41], v[174:177], v1, v1 op_sel_hi:[0,0,0]
	v_lshl_add_u64 v[226:227], s[54:55], 0, v[202:203]
	s_mov_b32 m0, s60
	s_nop 0
	global_load_lds_dwordx4 v[226:227], off
	v_mfma_scale_f32_16x16x128_f8f6f4 v[170:173], v[10:17], v[42:49], v[170:173], v1, v1 op_sel_hi:[0,0,0]
	v_mfma_scale_f32_16x16x128_f8f6f4 v[166:169], v[2:9], v[42:49], v[166:169], v1, v1 op_sel_hi:[0,0,0]
	v_mfma_scale_f32_16x16x128_f8f6f4 v[154:157], v[10:17], v[50:57], v[154:157], v1, v1 op_sel_hi:[0,0,0]
	v_mfma_scale_f32_16x16x128_f8f6f4 v[150:153], v[2:9], v[50:57], v[150:153], v1, v1 op_sel_hi:[0,0,0]
	v_mfma_scale_f32_16x16x128_f8f6f4 v[138:141], v[10:17], v[58:65], v[138:141], v1, v1 op_sel_hi:[0,0,0]
	v_mfma_scale_f32_16x16x128_f8f6f4 v[134:137], v[2:9], v[58:65], v[134:137], v1, v1 op_sel_hi:[0,0,0]
	s_setprio 0
	s_barrier
	v_lshl_add_u64 v[226:227], s[56:57], 0, v[200:201]
	s_add_i32 m0, s17, 0x18000
	s_nop 0
	global_load_lds_dwordx4 v[226:227], off
	s_add_i32 m0, s17, 0x1a000
	v_lshl_add_u64 v[226:227], s[56:57], 0, v[204:205]
	global_load_lds_dwordx4 v[226:227], off
	s_add_u32 s52, s52, 0x40100
	s_addc_u32 s53, s53, 0
	v_lshl_add_u64 v[226:227], s[52:53], 0, v[200:201]
	s_add_i32 m0, s17, 0x1c000
	v_lshl_add_u64 v[68:69], v[68:69], 0, s[12:13]
	global_load_lds_dwordx4 v[226:227], off
	v_lshl_add_u64 v[226:227], s[52:53], 0, v[204:205]
	s_add_i32 m0, s17, 0x1e000
	s_nop 0
	global_load_lds_dwordx4 v[226:227], off
	s_and_b64 vcc, exec, s[2:3]
	s_cbranch_vccnz .Lhalfskip_p8b
	ds_read_b128 v[58:61], v223 offset:49152
	ds_read_b128 v[62:65], v223 offset:50176
	ds_read_b128 v[50:53], v223 offset:51200
	ds_read_b128 v[54:57], v223 offset:52224
	ds_read_b128 v[42:45], v223 offset:53248
	ds_read_b128 v[46:49], v223 offset:54272
	ds_read_b128 v[34:37], v223 offset:55296
	ds_read_b128 v[38:41], v223 offset:56320
.Lhalfskip_p8b:
	s_waitcnt vmcnt(6)
	s_waitcnt lgkmcnt(0)
	s_cbranch_vccnz .Lp8_skip_dB
	s_barrier
	s_setprio 1
	v_mfma_scale_f32_16x16x128_f8f6f4 v[130:133], v[26:33], v[58:65], v[130:133], v1, v1 op_sel_hi:[0,0,0]
	v_mfma_scale_f32_16x16x128_f8f6f4 v[126:129], v[18:25], v[58:65], v[126:129], v1, v1 op_sel_hi:[0,0,0]
	v_mfma_scale_f32_16x16x128_f8f6f4 v[114:117], v[26:33], v[50:57], v[114:117], v1, v1 op_sel_hi:[0,0,0]
	v_mfma_scale_f32_16x16x128_f8f6f4 v[110:113], v[18:25], v[50:57], v[110:113], v1, v1 op_sel_hi:[0,0,0]
	v_mfma_scale_f32_16x16x128_f8f6f4 v[98:101], v[26:33], v[42:49], v[98:101], v1, v1 op_sel_hi:[0,0,0]
	v_mfma_scale_f32_16x16x128_f8f6f4 v[94:97], v[18:25], v[42:49], v[94:97], v1, v1 op_sel_hi:[0,0,0]
	v_mfma_scale_f32_16x16x128_f8f6f4 v[82:85], v[26:33], v[34:41], v[82:85], v1, v1 op_sel_hi:[0,0,0]
	v_mfma_scale_f32_16x16x128_f8f6f4 v[78:81], v[18:25], v[34:41], v[78:81], v1, v1 op_sel_hi:[0,0,0]
	s_setprio 0
	s_setprio 1
	v_mfma_scale_f32_16x16x128_f8f6f4 v[122:125], v[10:17], v[58:65], v[122:125], v1, v1 op_sel_hi:[0,0,0]
	v_mfma_scale_f32_16x16x128_f8f6f4 v[118:121], v[2:9], v[58:65], v[118:121], v1, v1 op_sel_hi:[0,0,0]
	v_mfma_scale_f32_16x16x128_f8f6f4 v[106:109], v[10:17], v[50:57], v[106:109], v1, v1 op_sel_hi:[0,0,0]
	s_mov_b32 m0, s62
	s_nop 0
	global_load_lds_dwordx4 v[68:69], off
	v_mfma_scale_f32_16x16x128_f8f6f4 v[102:105], v[2:9], v[50:57], v[102:105], v1, v1 op_sel_hi:[0,0,0]
	v_mfma_scale_f32_16x16x128_f8f6f4 v[90:93], v[10:17], v[42:49], v[90:93], v1, v1 op_sel_hi:[0,0,0]
	v_lshl_add_u64 v[68:69], v[212:213], 0, s[12:13]
	s_mov_b32 m0, s63
	s_nop 0
	global_load_lds_dwordx4 v[68:69], off
	v_mfma_scale_f32_16x16x128_f8f6f4 v[86:89], v[2:9], v[42:49], v[86:89], v1, v1 op_sel_hi:[0,0,0]
	v_mfma_scale_f32_16x16x128_f8f6f4 v[74:77], v[10:17], v[34:41], v[74:77], v1, v1 op_sel_hi:[0,0,0]
	v_mfma_scale_f32_16x16x128_f8f6f4 v[70:73], v[2:9], v[34:41], v[70:73], v1, v1 op_sel_hi:[0,0,0]
	s_setprio 0
	s_branch .LBB0_900
.Lp8_skip_bB:
	s_barrier
.Lp8_skip_b:
	v_lshl_add_u64 v[68:69], s[54:55], 0, v[198:199]
	s_mov_b32 m0, s17
	s_nop 0
	global_load_lds_dwordx4 v[68:69], off
	s_mov_b32 m0, s58
	s_nop 0
	global_load_lds_dwordx4 v[212:213], off
	s_branch .LBB0_903
.Lp8_skip_dB:
	s_barrier
.Lp8_skip_d:
	s_mov_b32 m0, s62
	s_nop 0
	global_load_lds_dwordx4 v[68:69], off
	v_lshl_add_u64 v[68:69], v[212:213], 0, s[12:13]
	s_mov_b32 m0, s63
	s_nop 0
	global_load_lds_dwordx4 v[68:69], off
	s_branch .LBB0_900
